# baseline (speedup 1.0000x reference)
_Z9qsim_mainPKDF16_PK15HIP_vector_typeIfLj2EEPf:
	s_cmpk_gt_i32 s2, 0x3ff
	s_cbranch_scc1 .LBB1_11
	s_load_dwordx4 s[8:11], s[0:1], 0x0
	s_load_dwordx2 s[4:5], s[0:1], 0x10
	s_mul_i32 s1, s2, 56
	s_mul_hi_i32 s0, s2, 56
	v_mbcnt_lo_u32_b32 v2, -1, 0
	s_waitcnt lgkmcnt(0)
	s_add_u32 s6, s8, 0x20000
	s_addc_u32 s7, s9, 0
	s_add_u32 s20, s8, 0x80000
	s_addc_u32 s21, s9, 0
	s_add_u32 s12, s8, 0x38000
	s_addc_u32 s13, s9, 0
	s_add_i32 s22, s2, 0xfffffe00
	s_add_u32 s14, s4, s1
	s_addc_u32 s15, s5, s0
	s_mul_hi_i32 s0, s2, 0xa00
	s_mulk_i32 s2, 0xa00
	v_mbcnt_hi_u32_b32 v161, -1, v2
	s_add_u32 s10, s10, s2
	v_and_b32_e32 v2, 64, v161
	s_addc_u32 s11, s11, s0
	v_mov_b32_e32 v155, 0
	s_movk_i32 s23, 0x1000
	s_mov_b64 s[16:17], 0x28000
	v_mov_b32_e32 v1, 0x10000
	s_movk_i32 s24, 0x100
	v_mov_b32_e32 v158, 0x60
	v_mov_b32_e32 v159, 0x280
	v_mov_b32_e32 v160, 0x1280
	s_mov_b64 s[18:19], 0x40000
	s_mov_b32 s25, 0x40000
	v_xor_b32_e32 v162, 32, v161
	v_add_u32_e32 v163, 64, v2
	v_xor_b32_e32 v164, 16, v161
	v_mov_b32_e32 v165, 0x10a00
	v_lshlrev_b32_e32 v195, 3, v0
	v_and_b32_e32 v196, 63, v0
	v_lshlrev_b32_e32 v196, 3, v196
	v_add_u32_e32 v194, 0x10000, v195
	global_load_dwordx2 v[190:191], v195, s[10:11]
	global_load_dwordx2 v[192:193], v196, s[10:11] offset:2048
	v_readfirstlane_b32 s35, v0
	s_waitcnt vmcnt(0)
	ds_write_b64 v194, v[190:191]
	s_cmp_lg_u32 s35, 0
	s_cbranch_scc1 .Lpro_skip
	ds_write_b64 v194, v[192:193] offset:2048
.Lpro_skip:
	s_waitcnt lgkmcnt(0)
	s_barrier
	s_branch .LBB1_3

.LBB1_3:
	v_mov_b32_e32 v156, v0
	s_nop 0
	v_ashrrev_i32_e32 v157, 31, v156
	v_and_b32_e32 v167, 63, v156
	v_lshlrev_b32_e32 v169, 3, v167
	s_cmp_lt_i32 s22, 0
	s_cbranch_scc0 .Lno_pref
	s_add_u32 s36, s10, 0x140000
	s_addc_u32 s37, s11, 0
	global_load_dwordx2 v[190:191], v195, s[36:37]
	global_load_dwordx2 v[192:193], v196, s[36:37] offset:2048
.Lno_pref:
	v_readfirstlane_b32 s4, v156
	s_ashr_i32 s27, s4, 7
	s_lshl_b32 s0, s27, 1
	s_ashr_i32 s1, s0, 31
	s_lshl_b64 s[2:3], s[0:1], 13
	s_add_u32 s2, s8, s2
	s_addc_u32 s3, s9, s3
	s_add_u32 s28, s2, 0x18000
	s_addc_u32 s29, s3, 0
	v_lshlrev_b32_e32 v154, 4, v167
	v_lshl_add_u64 v[6:7], s[28:29], 0, v[154:155]
	v_or_b32_e32 v8, 0x800, v169
	v_add_co_u32_e32 v6, vcc, s23, v6
	v_lshlrev_b32_e32 v168, 1, v8
	s_nop 0
	v_addc_co_u32_e32 v7, vcc, 0, v7, vcc
	v_lshl_add_u64 v[8:9], s[6:7], 0, v[154:155]
	global_load_dwordx4 v[150:153], v154, s[28:29]
	global_load_dwordx4 v[146:149], v154, s[28:29] offset:1024
	global_load_dwordx4 v[142:145], v154, s[28:29] offset:2048
	global_load_dwordx4 v[138:141], v154, s[28:29] offset:3072
	global_load_dwordx4 v[126:129], v[6:7], off offset:1024
	global_load_dwordx4 v[122:125], v[6:7], off offset:2048
	global_load_dwordx4 v[118:121], v154, s[6:7]
	global_load_dwordx4 v[114:117], v154, s[6:7] offset:1024
	global_load_dwordx4 v[110:113], v154, s[6:7] offset:2048
	global_load_dwordx4 v[106:109], v154, s[6:7] offset:3072
	global_load_dwordx4 v[134:137], v168, s[28:29]
	global_load_dwordx4 v[102:105], v168, s[6:7]
	v_add_co_u32_e32 v8, vcc, s23, v8
	s_nop 1
	v_addc_co_u32_e32 v9, vcc, 0, v9, vcc
	global_load_dwordx4 v[130:133], v[6:7], off offset:3072
	global_load_dwordx4 v[98:101], v[8:9], off offset:1024
	global_load_dwordx4 v[94:97], v[8:9], off offset:2048
	global_load_dwordx4 v[90:93], v[8:9], off offset:3072
	v_lshl_add_u64 v[6:7], s[2:3], 0, v[154:155]
	v_lshl_add_u64 v[8:9], v[6:7], 0, s[16:17]
	v_add_co_u32_e32 v6, vcc, 0x28000, v6
	s_nop 1
	v_addc_co_u32_e32 v7, vcc, 0, v7, vcc
	global_load_dwordx4 v[86:89], v[6:7], off
	global_load_dwordx4 v[82:85], v[8:9], off offset:1024
	v_cmp_gt_i32_e32 vcc, 16, v156
	v_lshl_add_u32 v166, v156, 2, v165
	s_and_saveexec_b64 s[2:3], vcc
	ds_write_b32 v166, v155
	s_or_b64 exec, exec, s[2:3]
	v_mov_b32_e32 v10, v167
	s_ashr_i32 s2, s4, 6
	v_ashrrev_i32_e32 v11, 5, v10
	v_and_b32_e32 v2, 3, v10
	v_lshlrev_b32_e32 v4, 2, v10
	v_lshl_add_u32 v34, v11, 9, v1
	v_lshlrev_b32_e32 v2, 3, v2
	v_and_b32_e32 v4, 32, v4
	v_and_b32_e32 v3, 16, v10
	v_or3_b32 v2, v34, v2, v4
	v_lshlrev_b32_e32 v4, 4, v10
	s_cmpk_lt_u32 s4, 0x80
	v_and_b32_e32 v4, 64, v4
	v_lshlrev_b32_e32 v3, 3, v3
	s_cselect_b32 s3, 0, 15
	v_or3_b32 v15, v2, v4, v3
	v_bitop3_b32 v2, v10, s3, 15 bitop3:0x6c
	v_lshlrev_b32_e32 v2, 3, v2
	v_or_b32_e32 v3, 0x10800, v2
	v_or_b32_e32 v4, 0x10880, v2
	v_or_b32_e32 v6, 0x10900, v2
	v_or_b32_e32 v8, 0x10980, v2
	ds_read_b64 v[2:3], v3
	ds_read_b64 v[4:5], v4
	ds_read_b64 v[6:7], v6
	ds_read_b64 v[8:9], v8
	v_and_b32_e32 v16, 31, v10
	v_cmp_gt_u32_e32 vcc, 16, v16
	v_lshrrev_b32_e32 v12, 1, v10
	v_lshlrev_b32_e32 v13, 1, v10
	s_waitcnt lgkmcnt(3)
	v_cndmask_b32_e32 v16, v3, v2, vcc
	v_cndmask_b32_e64 v2, v2, -v3, vcc
	s_waitcnt lgkmcnt(2)
	v_cndmask_b32_e64 v3, v4, -v5, vcc
	v_cndmask_b32_e32 v18, v5, v4, vcc
	s_waitcnt lgkmcnt(1)
	v_cndmask_b32_e64 v4, v6, -v7, vcc
	s_waitcnt lgkmcnt(0)
	v_cndmask_b32_e64 v5, v8, -v9, vcc
	v_cvt_pk_f16_f32 v20, v2, v3
	v_lshrrev_b32_e32 v2, 1, v11
	v_cvt_pk_f16_f32 v21, v4, v5
	v_lshrrev_b32_e32 v3, 2, v10
	v_xor_b32_e32 v5, v12, v11
	v_xor_b32_e32 v2, v2, v10
	v_xor_b32_e32 v3, v3, v11
	v_and_b32_e32 v4, 2, v13
	v_lshlrev_b32_e32 v5, 2, v5
	v_lshlrev_b32_e32 v2, 3, v2
	v_bfe_i32 v14, v10, 4, 1
	v_and_b32_e32 v17, 15, v10
	v_and_b32_e32 v5, 4, v5
	v_and_b32_e32 v2, 8, v2
	v_and_or_b32 v3, v3, 1, v4
	v_lshlrev_b32_e32 v4, 8, v11
	s_lshl_b32 s3, s2, 3
	v_cndmask_b32_e32 v19, v7, v6, vcc
	v_or3_b32 v2, v3, v5, v2
	v_lshlrev_b32_e32 v3, 11, v17
	v_and_b32_e32 v5, 0x200, v4
	v_and_b32_e32 v4, 0x100, v4
	v_bitop3_b32 v6, s3, v14, 31 bitop3:0x78
	v_or3_b32 v12, v5, v3, v4
	v_lshlrev_b32_e32 v13, 4, v2
	ds_read2_b64 v[2:5], v15 offset1:32
	v_lshl_add_u32 v6, v6, 3, v34
	v_cndmask_b32_e32 v22, v9, v8, vcc
	ds_read2_b64 v[6:9], v6 offset0:128 offset1:160
	v_cvt_pk_f16_f32 v19, v19, v22
	s_waitcnt lgkmcnt(1)
	v_mov_b32_e32 v24, v3
	v_mov_b32_e32 v25, v5
	v_pk_mov_b32 v[28:29], v[4:5], v[2:3] op_sel:[1,0]
	v_cvt_pk_f16_f32 v18, v16, v18
	v_lshlrev_b32_e32 v16, 11, v10
	v_mov_b32_e32 v22, v2
	v_mov_b32_e32 v23, v4
	s_waitcnt lgkmcnt(0)
	v_pk_mul_f32 v[10:11], v[6:7], v[24:25] op_sel:[1,0]
	v_pk_mov_b32 v[26:27], v[2:3], v[4:5] op_sel:[1,0]
	v_pk_mul_f32 v[2:3], v[6:7], v[28:29]
	v_pk_mul_f32 v[4:5], v[8:9], v[24:25] op_sel:[1,0]
	v_pk_fma_f32 v[10:11], v[6:7], v[22:23], v[10:11] op_sel_hi:[0,1,1] neg_lo:[0,0,1] neg_hi:[0,0,1]
	v_pk_fma_f32 v[2:3], v[6:7], v[26:27], v[2:3] op_sel:[0,0,1] op_sel_hi:[1,1,0]
	v_pk_fma_f32 v[6:7], v[8:9], v[22:23], v[4:5] op_sel_hi:[0,1,1] neg_lo:[0,0,1] neg_hi:[0,0,1]
	v_pk_mul_f32 v[4:5], v[8:9], v[28:29]
	v_and_b32_e32 v36, 31, v14
	v_pk_fma_f32 v[4:5], v[8:9], v[26:27], v[4:5] op_sel:[0,0,1] op_sel_hi:[1,1,0]
	s_and_b32 s5, s3, 8
	v_cvt_pk_f16_f32 v5, v4, v5
	v_cvt_pk_f16_f32 v4, v2, v3
	v_cvt_pk_f16_f32 v3, v6, v7
	v_cvt_pk_f16_f32 v2, v10, v11
	v_and_b32_e32 v6, 0x8000, v16
	v_or3_b32 v35, v13, v12, v6
	v_mfma_f32_32x32x16_f16 v[2:17], v[2:5], v[18:21], 0
	s_bfe_u32 s26, s2, 0x10001
	s_or_b32 s5, s26, s5
	s_lshl_b32 s26, s2, 9
	s_and_b32 s26, s26, 0x400
	s_lshl_b32 s5, s5, 4
	v_mov_b32_e32 v30, s26
	v_bitop3_b32 v37, s5, v35, v30 bitop3:0x36
	s_nop 4
	v_cvt_pk_f16_f32 v9, v8, v9
	v_cvt_pk_f16_f32 v8, v6, v7
	v_cvt_pk_f16_f32 v7, v4, v5
	v_bitop3_b32 v4, s3, v36, 1 bitop3:0x36
	v_lshl_add_u32 v4, v4, 3, v34
	ds_read2_b64 v[30:33], v4 offset0:128 offset1:160
	v_cvt_pk_f16_f32 v6, v2, v3
	ds_write_b128 v37, v[6:9]
	v_cvt_pk_f16_f32 v4, v14, v15
	v_cvt_pk_f16_f32 v5, v16, v17
	s_waitcnt lgkmcnt(1)
	v_pk_mul_f32 v[8:9], v[32:33], v[24:25] op_sel:[1,0]
	v_pk_mul_f32 v[2:3], v[30:31], v[24:25] op_sel:[1,0]
	v_pk_mul_f32 v[6:7], v[30:31], v[28:29]
	v_pk_fma_f32 v[14:15], v[32:33], v[22:23], v[8:9] op_sel_hi:[0,1,1] neg_lo:[0,0,1] neg_hi:[0,0,1]
	v_pk_mul_f32 v[8:9], v[32:33], v[28:29]
	v_pk_fma_f32 v[2:3], v[30:31], v[22:23], v[2:3] op_sel_hi:[0,1,1] neg_lo:[0,0,1] neg_hi:[0,0,1]
	v_pk_fma_f32 v[6:7], v[30:31], v[26:27], v[6:7] op_sel:[0,0,1] op_sel_hi:[1,1,0]
	v_pk_fma_f32 v[8:9], v[32:33], v[26:27], v[8:9] op_sel:[0,0,1] op_sel_hi:[1,1,0]
	v_xor_b32_e32 v38, 16, v37
	v_cvt_pk_f16_f32 v9, v8, v9
	v_cvt_pk_f16_f32 v8, v6, v7
	v_cvt_pk_f16_f32 v7, v14, v15
	v_cvt_pk_f16_f32 v6, v2, v3
	v_cvt_pk_f16_f32 v3, v12, v13
	v_cvt_pk_f16_f32 v2, v10, v11
	v_xor_b32_e32 v10, 0x280, v37
	ds_write_b128 v10, v[2:5]
	v_mfma_f32_32x32x16_f16 v[2:17], v[6:9], v[18:21], 0
	s_or_b32 s28, s5, s26
	s_nop 10
	v_cvt_pk_f16_f32 v9, v8, v9
	v_cvt_pk_f16_f32 v8, v6, v7
	v_cvt_pk_f16_f32 v7, v4, v5
	v_bitop3_b32 v4, s3, v36, 2 bitop3:0x36
	v_lshl_add_u32 v4, v4, 3, v34
	ds_read2_b64 v[30:33], v4 offset0:128 offset1:160
	v_cvt_pk_f16_f32 v6, v2, v3
	ds_write_b128 v38, v[6:9]
	v_cvt_pk_f16_f32 v4, v14, v15
	v_cvt_pk_f16_f32 v5, v16, v17
	s_waitcnt lgkmcnt(1)
	v_pk_mul_f32 v[8:9], v[32:33], v[24:25] op_sel:[1,0]
	v_pk_mul_f32 v[2:3], v[30:31], v[24:25] op_sel:[1,0]
	v_pk_mul_f32 v[6:7], v[30:31], v[28:29]
	v_pk_fma_f32 v[14:15], v[32:33], v[22:23], v[8:9] op_sel_hi:[0,1,1] neg_lo:[0,0,1] neg_hi:[0,0,1]
	v_pk_mul_f32 v[8:9], v[32:33], v[28:29]
	v_pk_fma_f32 v[2:3], v[30:31], v[22:23], v[2:3] op_sel_hi:[0,1,1] neg_lo:[0,0,1] neg_hi:[0,0,1]
	v_pk_fma_f32 v[6:7], v[30:31], v[26:27], v[6:7] op_sel:[0,0,1] op_sel_hi:[1,1,0]
	v_pk_fma_f32 v[8:9], v[32:33], v[26:27], v[8:9] op_sel:[0,0,1] op_sel_hi:[1,1,0]
	v_bitop3_b32 v38, s28, v35, 32 bitop3:0x36
	v_cvt_pk_f16_f32 v9, v8, v9
	v_cvt_pk_f16_f32 v8, v6, v7
	v_cvt_pk_f16_f32 v7, v14, v15
	v_cvt_pk_f16_f32 v6, v2, v3
	v_cvt_pk_f16_f32 v3, v12, v13
	v_cvt_pk_f16_f32 v2, v10, v11
	v_xor_b32_e32 v10, 0x290, v37
	ds_write_b128 v10, v[2:5]
	v_mfma_f32_32x32x16_f16 v[2:17], v[6:9], v[18:21], 0
	s_nop 11
	v_cvt_pk_f16_f32 v9, v8, v9
	v_cvt_pk_f16_f32 v8, v6, v7
	v_cvt_pk_f16_f32 v7, v4, v5
	v_bitop3_b32 v4, s3, v36, 3 bitop3:0x36
	v_lshl_add_u32 v4, v4, 3, v34
	ds_read2_b64 v[30:33], v4 offset0:128 offset1:160
	v_cvt_pk_f16_f32 v6, v2, v3
	ds_write_b128 v38, v[6:9]
	v_cvt_pk_f16_f32 v4, v14, v15
	v_cvt_pk_f16_f32 v5, v16, v17
	s_waitcnt lgkmcnt(1)
	v_pk_mul_f32 v[8:9], v[32:33], v[24:25] op_sel:[1,0]
	v_pk_mul_f32 v[2:3], v[30:31], v[24:25] op_sel:[1,0]
	v_pk_mul_f32 v[6:7], v[30:31], v[28:29]
	v_pk_fma_f32 v[14:15], v[32:33], v[22:23], v[8:9] op_sel_hi:[0,1,1] neg_lo:[0,0,1] neg_hi:[0,0,1]
	v_pk_mul_f32 v[8:9], v[32:33], v[28:29]
	v_pk_fma_f32 v[2:3], v[30:31], v[22:23], v[2:3] op_sel_hi:[0,1,1] neg_lo:[0,0,1] neg_hi:[0,0,1]
	v_pk_fma_f32 v[6:7], v[30:31], v[26:27], v[6:7] op_sel:[0,0,1] op_sel_hi:[1,1,0]
	v_pk_fma_f32 v[8:9], v[32:33], v[26:27], v[8:9] op_sel:[0,0,1] op_sel_hi:[1,1,0]
	s_nop 0
	v_cvt_pk_f16_f32 v9, v8, v9
	v_cvt_pk_f16_f32 v8, v6, v7
	v_cvt_pk_f16_f32 v7, v14, v15
	v_cvt_pk_f16_f32 v6, v2, v3
	v_cvt_pk_f16_f32 v3, v12, v13
	v_cvt_pk_f16_f32 v2, v10, v11
	v_xor_b32_e32 v10, 0x280, v38
	ds_write_b128 v10, v[2:5]
	v_mfma_f32_32x32x16_f16 v[2:17], v[6:9], v[18:21], 0
	v_xor_b32_e32 v38, 48, v37
	s_nop 10
	v_cvt_pk_f16_f32 v9, v8, v9
	v_cvt_pk_f16_f32 v8, v6, v7
	v_cvt_pk_f16_f32 v7, v4, v5
	v_bitop3_b32 v4, s3, v36, 4 bitop3:0x36
	v_lshl_add_u32 v4, v4, 3, v34
	ds_read2_b64 v[30:33], v4 offset0:128 offset1:160
	v_cvt_pk_f16_f32 v6, v2, v3
	ds_write_b128 v38, v[6:9]
	v_cvt_pk_f16_f32 v4, v14, v15
	v_cvt_pk_f16_f32 v5, v16, v17
	s_waitcnt lgkmcnt(1)
	v_pk_mul_f32 v[8:9], v[32:33], v[24:25] op_sel:[1,0]
	v_pk_mul_f32 v[2:3], v[30:31], v[24:25] op_sel:[1,0]
	v_pk_mul_f32 v[6:7], v[30:31], v[28:29]
	v_pk_fma_f32 v[14:15], v[32:33], v[22:23], v[8:9] op_sel_hi:[0,1,1] neg_lo:[0,0,1] neg_hi:[0,0,1]
	v_pk_mul_f32 v[8:9], v[32:33], v[28:29]
	v_pk_fma_f32 v[2:3], v[30:31], v[22:23], v[2:3] op_sel_hi:[0,1,1] neg_lo:[0,0,1] neg_hi:[0,0,1]
	v_pk_fma_f32 v[6:7], v[30:31], v[26:27], v[6:7] op_sel:[0,0,1] op_sel_hi:[1,1,0]
	v_pk_fma_f32 v[8:9], v[32:33], v[26:27], v[8:9] op_sel:[0,0,1] op_sel_hi:[1,1,0]
	v_bitop3_b32 v38, s28, v35, 64 bitop3:0x36
	v_cvt_pk_f16_f32 v9, v8, v9
	v_cvt_pk_f16_f32 v8, v6, v7
	v_cvt_pk_f16_f32 v7, v14, v15
	v_cvt_pk_f16_f32 v6, v2, v3
	v_cvt_pk_f16_f32 v3, v12, v13
	v_cvt_pk_f16_f32 v2, v10, v11
	v_xor_b32_e32 v10, 0x2b0, v37
	ds_write_b128 v10, v[2:5]
	v_mfma_f32_32x32x16_f16 v[2:17], v[6:9], v[18:21], 0
	v_bitop3_b32 v35, s28, v35, v158 bitop3:0x36
	s_nop 10
	v_cvt_pk_f16_f32 v9, v8, v9
	v_cvt_pk_f16_f32 v8, v6, v7
	v_cvt_pk_f16_f32 v7, v4, v5
	v_bitop3_b32 v4, s3, v36, 5 bitop3:0x36
	v_lshl_add_u32 v4, v4, 3, v34
	ds_read2_b64 v[30:33], v4 offset0:128 offset1:160
	v_cvt_pk_f16_f32 v6, v2, v3
	ds_write_b128 v38, v[6:9]
	v_cvt_pk_f16_f32 v4, v14, v15
	v_cvt_pk_f16_f32 v5, v16, v17
	s_waitcnt lgkmcnt(1)
	v_pk_mul_f32 v[8:9], v[32:33], v[24:25] op_sel:[1,0]
	v_pk_mul_f32 v[2:3], v[30:31], v[24:25] op_sel:[1,0]
	v_pk_mul_f32 v[6:7], v[30:31], v[28:29]
	v_pk_fma_f32 v[14:15], v[32:33], v[22:23], v[8:9] op_sel_hi:[0,1,1] neg_lo:[0,0,1] neg_hi:[0,0,1]
	v_pk_mul_f32 v[8:9], v[32:33], v[28:29]
	v_pk_fma_f32 v[2:3], v[30:31], v[22:23], v[2:3] op_sel_hi:[0,1,1] neg_lo:[0,0,1] neg_hi:[0,0,1]
	v_pk_fma_f32 v[6:7], v[30:31], v[26:27], v[6:7] op_sel:[0,0,1] op_sel_hi:[1,1,0]
	v_pk_fma_f32 v[8:9], v[32:33], v[26:27], v[8:9] op_sel:[0,0,1] op_sel_hi:[1,1,0]
	s_nop 0
	v_cvt_pk_f16_f32 v9, v8, v9
	v_cvt_pk_f16_f32 v8, v6, v7
	v_cvt_pk_f16_f32 v7, v14, v15
	v_cvt_pk_f16_f32 v6, v2, v3
	v_cvt_pk_f16_f32 v3, v12, v13
	v_cvt_pk_f16_f32 v2, v10, v11
	v_xor_b32_e32 v10, 0x280, v38
	ds_write_b128 v10, v[2:5]
	v_mfma_f32_32x32x16_f16 v[2:17], v[6:9], v[18:21], 0
	v_xor_b32_e32 v38, 0x50, v37
	s_nop 10
	v_cvt_pk_f16_f32 v9, v8, v9
	v_cvt_pk_f16_f32 v8, v6, v7
	v_cvt_pk_f16_f32 v7, v4, v5
	v_bitop3_b32 v4, s3, v36, 6 bitop3:0x36
	v_lshl_add_u32 v4, v4, 3, v34
	ds_read2_b64 v[30:33], v4 offset0:128 offset1:160
	v_cvt_pk_f16_f32 v6, v2, v3
	ds_write_b128 v38, v[6:9]
	v_cvt_pk_f16_f32 v4, v14, v15
	v_cvt_pk_f16_f32 v5, v16, v17
	s_waitcnt lgkmcnt(1)
	v_pk_mul_f32 v[8:9], v[32:33], v[24:25] op_sel:[1,0]
	v_pk_mul_f32 v[2:3], v[30:31], v[24:25] op_sel:[1,0]
	v_pk_mul_f32 v[6:7], v[30:31], v[28:29]
	v_pk_fma_f32 v[14:15], v[32:33], v[22:23], v[8:9] op_sel_hi:[0,1,1] neg_lo:[0,0,1] neg_hi:[0,0,1]
	v_pk_mul_f32 v[8:9], v[32:33], v[28:29]
	v_pk_fma_f32 v[2:3], v[30:31], v[22:23], v[2:3] op_sel_hi:[0,1,1] neg_lo:[0,0,1] neg_hi:[0,0,1]
	v_pk_fma_f32 v[6:7], v[30:31], v[26:27], v[6:7] op_sel:[0,0,1] op_sel_hi:[1,1,0]
	v_pk_fma_f32 v[8:9], v[32:33], v[26:27], v[8:9] op_sel:[0,0,1] op_sel_hi:[1,1,0]
	s_nop 0
	v_cvt_pk_f16_f32 v9, v8, v9
	v_cvt_pk_f16_f32 v8, v6, v7
	v_cvt_pk_f16_f32 v7, v14, v15
	v_cvt_pk_f16_f32 v6, v2, v3
	v_cvt_pk_f16_f32 v3, v12, v13
	v_cvt_pk_f16_f32 v2, v10, v11
	v_xor_b32_e32 v10, 0x2d0, v37
	ds_write_b128 v10, v[2:5]
	v_mfma_f32_32x32x16_f16 v[2:17], v[6:9], v[18:21], 0
	s_nop 11
	v_cvt_pk_f16_f32 v9, v8, v9
	v_cvt_pk_f16_f32 v8, v6, v7
	v_cvt_pk_f16_f32 v7, v4, v5
	v_bitop3_b32 v4, s3, v36, 7 bitop3:0x36
	v_lshl_add_u32 v4, v4, 3, v34
	ds_read2_b64 v[30:33], v4 offset0:128 offset1:160
	v_cvt_pk_f16_f32 v6, v2, v3
	ds_write_b128 v35, v[6:9]
	v_cvt_pk_f16_f32 v4, v14, v15
	v_cvt_pk_f16_f32 v5, v16, v17
	s_waitcnt lgkmcnt(1)
	v_pk_mul_f32 v[8:9], v[32:33], v[24:25] op_sel:[1,0]
	v_pk_mul_f32 v[2:3], v[30:31], v[24:25] op_sel:[1,0]
	v_pk_mul_f32 v[6:7], v[30:31], v[28:29]
	v_pk_fma_f32 v[14:15], v[32:33], v[22:23], v[8:9] op_sel_hi:[0,1,1] neg_lo:[0,0,1] neg_hi:[0,0,1]
	v_pk_mul_f32 v[8:9], v[32:33], v[28:29]
	v_pk_fma_f32 v[2:3], v[30:31], v[22:23], v[2:3] op_sel_hi:[0,1,1] neg_lo:[0,0,1] neg_hi:[0,0,1]
	v_pk_fma_f32 v[6:7], v[30:31], v[26:27], v[6:7] op_sel:[0,0,1] op_sel_hi:[1,1,0]
	v_pk_fma_f32 v[8:9], v[32:33], v[26:27], v[8:9] op_sel:[0,0,1] op_sel_hi:[1,1,0]
	s_nop 0
	v_cvt_pk_f16_f32 v9, v8, v9
	v_cvt_pk_f16_f32 v8, v6, v7
	v_cvt_pk_f16_f32 v7, v14, v15
	v_cvt_pk_f16_f32 v6, v2, v3
	v_cvt_pk_f16_f32 v3, v12, v13
	v_cvt_pk_f16_f32 v2, v10, v11
	v_xor_b32_e32 v10, 0x280, v35
	ds_write_b128 v10, v[2:5]
	v_mfma_f32_32x32x16_f16 v[2:17], v[6:9], v[18:21], 0
	v_xor_b32_e32 v18, 0x70, v37
	s_nop 10
	v_cvt_pk_f16_f32 v9, v8, v9
	v_cvt_pk_f16_f32 v8, v6, v7
	v_cvt_pk_f16_f32 v7, v4, v5
	v_cvt_pk_f16_f32 v6, v2, v3
	ds_write_b128 v18, v[6:9]
	v_cvt_pk_f16_f32 v5, v16, v17
	v_cvt_pk_f16_f32 v4, v14, v15
	v_cvt_pk_f16_f32 v3, v12, v13
	v_cvt_pk_f16_f32 v2, v10, v11
	v_xor_b32_e32 v6, 0x2f0, v37
	ds_write_b128 v6, v[2:5]
	s_waitcnt lgkmcnt(0)
	s_barrier
	s_setprio 1
	v_lshrrev_b32_e32 v182, 5, v167
	v_bfe_u32 v2, v156, 4, 1
	v_bitop3_b32 v3, v182, v156, 1 bitop3:0x78
	v_lshlrev_b32_e32 v154, 2, v182
	v_xor_b32_e32 v3, v3, v2
	v_bitop3_b32 v4, v154, v156, 4 bitop3:0x78
	v_and_b32_e32 v5, 10, v156
	v_or3_b32 v3, v5, v4, v3
	s_lshl_b32 s5, s2, 4
	v_lshlrev_b32_e32 v3, 4, v3
	s_lshl_b32 s3, s2, 13
	s_and_b32 s29, s5, 16
	v_lshlrev_b32_e32 v170, 8, v182
	v_lshl_or_b32 v171, v2, 10, v3
	s_or_b32 s26, s29, s3
	v_bitop3_b32 v179, v171, s26, v170 bitop3:0x36
	ds_read_b128 v[18:21], v179
	ds_read_b128 v[22:25], v179 offset:32768
	s_waitcnt vmcnt(17) lgkmcnt(1)
	v_mfma_f32_32x32x16_f16 v[2:17], v[18:21], v[150:153], 0
	s_or_b32 s5, s26, 0x280
	v_bitop3_b32 v178, v171, s5, v170 bitop3:0x36
	s_or_b32 s30, s3, 0x800
	s_or_b32 s5, s29, s30
	s_or_b32 s31, s5, 0xa0
	s_or_b32 s5, s5, 0x220
	s_or_b32 s33, s3, 0x1000
	s_waitcnt vmcnt(7)
	v_mfma_f32_32x32x16_f16 v[34:49], v[18:21], v[134:137], 0
	ds_read_b128 v[18:21], v178
	ds_read_b128 v[26:29], v178 offset:32768
	s_or_b32 s29, s29, 64
	s_or_b32 s34, s29, s33
	v_bitop3_b32 v180, v171, s34, v170 bitop3:0x36
	s_or_b32 s29, s3, s29
	s_or_b32 s29, s29, 0x1280
	s_waitcnt lgkmcnt(1)
	v_mfma_f32_32x32x16_f16 v[2:17], v[18:21], v[146:149], v[2:17]
	v_mfma_f32_32x32x16_f16 v[2:17], v[22:25], v[142:145], v[2:17]
	v_mfma_f32_32x32x16_f16 v[34:49], v[18:21], v[126:129], v[34:49]
	s_waitcnt lgkmcnt(0)
	v_mfma_f32_32x32x16_f16 v[2:17], v[26:29], v[138:141], v[2:17]
	v_mfma_f32_32x32x16_f16 v[34:49], v[22:25], v[122:125], v[34:49]
	s_nop 10
	v_cvt_pk_f16_f32 v9, v8, v9
	v_cvt_pk_f16_f32 v8, v6, v7
	v_cvt_pk_f16_f32 v7, v4, v5
	v_cvt_pk_f16_f32 v6, v2, v3
	v_cvt_pk_f16_f32 v5, v16, v17
	v_cvt_pk_f16_f32 v4, v14, v15
	v_cvt_pk_f16_f32 v3, v12, v13
	s_waitcnt vmcnt(5)
	v_mfma_f32_32x32x16_f16 v[34:49], v[26:29], v[130:133], v[34:49]
	v_cvt_pk_f16_f32 v2, v10, v11
	v_mfma_f32_32x32x16_f16 v[18:33], v[6:9], v[118:121], 0
	s_nop 9
	v_cvt_pk_f16_f32 v13, v40, v41
	v_cvt_pk_f16_f32 v12, v38, v39
	v_cvt_pk_f16_f32 v11, v36, v37
	v_cvt_pk_f16_f32 v10, v34, v35
	v_cvt_pk_f16_f32 v17, v48, v49
	v_cvt_pk_f16_f32 v16, v46, v47
	v_cvt_pk_f16_f32 v15, v44, v45
	v_mfma_f32_32x32x16_f16 v[50:65], v[6:9], v[102:105], 0
	v_bitop3_b32 v6, v171, s31, v170 bitop3:0x36
	v_cvt_pk_f16_f32 v14, v42, v43
	v_mfma_f32_32x32x16_f16 v[18:33], v[2:5], v[114:117], v[18:33]
	s_waitcnt vmcnt(4)
	v_mfma_f32_32x32x16_f16 v[50:65], v[2:5], v[98:101], v[50:65]
	ds_read_b128 v[2:5], v6
	ds_read_b128 v[6:9], v6 offset:32768
	v_mfma_f32_32x32x16_f16 v[18:33], v[10:13], v[110:113], v[18:33]
	s_waitcnt vmcnt(3)
	v_mfma_f32_32x32x16_f16 v[50:65], v[10:13], v[94:97], v[50:65]
	s_waitcnt lgkmcnt(1)
	v_mfma_f32_32x32x16_f16 v[34:49], v[2:5], v[150:153], 0
	v_mfma_f32_32x32x16_f16 v[18:33], v[14:17], v[106:109], v[18:33]
	s_waitcnt vmcnt(2)
	v_mfma_f32_32x32x16_f16 v[50:65], v[14:17], v[90:93], v[50:65]
	v_bitop3_b32 v14, v171, s5, v170 bitop3:0x36
	ds_read_b128 v[10:13], v14
	ds_read_b128 v[14:17], v14 offset:32768
	s_and_b32 s5, s2, 1
	s_lshl_b32 s31, s5, 4
	s_or_b32 s2, s31, s3
	v_bitop3_b32 v173, v171, s2, v170 bitop3:0x36
	s_nop 2
	v_cvt_pk_f16_f32 v25, v24, v25
	s_waitcnt lgkmcnt(1)
	v_mfma_f32_32x32x16_f16 v[34:49], v[10:13], v[146:149], v[34:49]
	v_cvt_pk_f16_f32 v24, v22, v23
	v_cvt_pk_f16_f32 v23, v20, v21
	v_cvt_pk_f16_f32 v22, v18, v19
	v_cvt_pk_f16_f32 v21, v32, v33
	v_cvt_pk_f16_f32 v20, v30, v31
	v_cvt_pk_f16_f32 v19, v28, v29
	v_cvt_pk_f16_f32 v18, v26, v27
	v_mfma_f32_32x32x16_f16 v[34:49], v[6:9], v[142:145], v[34:49]
	ds_write_b128 v173, v[22:25]
	v_mfma_f32_32x32x16_f16 v[66:81], v[2:5], v[134:137], 0
	s_waitcnt lgkmcnt(1)
	v_mfma_f32_32x32x16_f16 v[34:49], v[14:17], v[138:141], v[34:49]
	v_mfma_f32_32x32x16_f16 v[66:81], v[10:13], v[126:129], v[66:81]
	s_nop 10
	v_cvt_pk_f16_f32 v41, v40, v41
	v_cvt_pk_f16_f32 v40, v38, v39
	v_cvt_pk_f16_f32 v38, v34, v35
	v_bitop3_b32 v34, v156, 31, v156 bitop3:0xc
	v_cvt_pk_f16_f32 v39, v36, v37
	v_lshrrev_b32_e32 v35, 4, v34
	v_bitop3_b32 v36, v34, v182, 1 bitop3:0x6c
	v_mfma_f32_32x32x16_f16 v[66:81], v[6:9], v[122:125], v[66:81]
	v_xor_b32_e32 v36, v36, v35
	v_bitop3_b32 v34, v34, v154, 4 bitop3:0x6c
	v_bitop3_b32 v37, v156, 10, 31 bitop3:8
	v_or3_b32 v34, v37, v34, v36
	v_lshlrev_b32_e32 v35, 10, v35
	v_lshlrev_b32_e32 v34, 4, v34
	v_or3_b32 v154, v35, v34, v170
	v_bitop3_b32 v172, s2, v154, v159 bitop3:0x36
	ds_write_b128 v172, v[18:21]
	v_cvt_pk_f16_f32 v21, v56, v57
	v_cvt_pk_f16_f32 v20, v54, v55
	v_cvt_pk_f16_f32 v19, v52, v53
	v_cvt_pk_f16_f32 v18, v50, v51
	v_mfma_f32_32x32x16_f16 v[66:81], v[14:17], v[130:133], v[66:81]
	v_cvt_pk_f16_f32 v177, v48, v49
	v_cvt_pk_f16_f32 v176, v46, v47
	v_cvt_pk_f16_f32 v175, v44, v45
	v_cvt_pk_f16_f32 v174, v42, v43
	ds_write_b128 v173, v[18:21] offset:32768
	v_cvt_pk_f16_f32 v21, v64, v65
	v_cvt_pk_f16_f32 v20, v62, v63
	v_mfma_f32_32x32x16_f16 v[2:17], v[38:41], v[118:121], 0
	v_cvt_pk_f16_f32 v19, v60, v61
	v_cvt_pk_f16_f32 v18, v58, v59
	ds_write_b128 v172, v[18:21] offset:32768
	ds_read_b128 v[18:21], v180
	ds_read_b128 v[22:25], v180 offset:32768
	v_cvt_pk_f16_f32 v73, v72, v73
	v_cvt_pk_f16_f32 v72, v70, v71
	v_mfma_f32_32x32x16_f16 v[34:49], v[38:41], v[102:105], 0
	v_cvt_pk_f16_f32 v71, v68, v69
	v_cvt_pk_f16_f32 v70, v66, v67
	v_cvt_pk_f16_f32 v69, v80, v81
	v_cvt_pk_f16_f32 v68, v78, v79
	v_cvt_pk_f16_f32 v67, v76, v77
	v_cvt_pk_f16_f32 v66, v74, v75
	v_mfma_f32_32x32x16_f16 v[2:17], v[174:177], v[114:117], v[2:17]
	v_mfma_f32_32x32x16_f16 v[34:49], v[174:177], v[98:101], v[34:49]
	v_bitop3_b32 v176, v171, s29, v170 bitop3:0x36
	ds_read_b128 v[26:29], v176
	ds_read_b128 v[30:33], v176 offset:32768
	s_or_b32 s29, s31, s30
	s_or_b32 s29, s29, 0xa0
	v_bitop3_b32 v175, v171, s29, v170 bitop3:0x36
	s_or_b32 s29, s2, 0xaa0
	s_xor_b32 s29, s29, 0x80
	s_waitcnt lgkmcnt(3)
	v_mfma_f32_32x32x16_f16 v[50:65], v[18:21], v[150:153], 0
	v_xor_b32_e32 v174, s29, v154
	s_or_b32 s29, s26, 0x18e0
	v_bitop3_b32 v181, v171, s29, v170 bitop3:0x36
	s_or_b32 s29, s26, 0x1a60
	v_bitop3_b32 v177, v171, s29, v170 bitop3:0x36
	s_or_b32 s29, s31, 64
	s_or_b32 s3, s3, s29
	v_mfma_f32_32x32x16_f16 v[2:17], v[70:73], v[110:113], v[2:17]
	s_or_b32 s29, s29, s33
	v_mfma_f32_32x32x16_f16 v[34:49], v[70:73], v[94:97], v[34:49]
	s_waitcnt lgkmcnt(1)
	v_mfma_f32_32x32x16_f16 v[50:65], v[26:29], v[146:149], v[50:65]
	v_mfma_f32_32x32x16_f16 v[2:17], v[66:69], v[106:109], v[2:17]
	v_mfma_f32_32x32x16_f16 v[34:49], v[66:69], v[90:93], v[34:49]
	s_nop 10
	v_cvt_pk_f16_f32 v9, v8, v9
	v_cvt_pk_f16_f32 v8, v6, v7
	v_cvt_pk_f16_f32 v7, v4, v5
	v_cvt_pk_f16_f32 v6, v2, v3
	v_cvt_pk_f16_f32 v5, v16, v17
	v_cvt_pk_f16_f32 v4, v14, v15
	v_cvt_pk_f16_f32 v3, v12, v13
	v_mfma_f32_32x32x16_f16 v[66:81], v[18:21], v[134:137], 0
	v_cvt_pk_f16_f32 v2, v10, v11
	ds_write_b128 v175, v[6:9]
	ds_write_b128 v174, v[2:5]
	v_cvt_pk_f16_f32 v5, v40, v41
	v_cvt_pk_f16_f32 v4, v38, v39
	v_cvt_pk_f16_f32 v3, v36, v37
	v_cvt_pk_f16_f32 v2, v34, v35
	v_mfma_f32_32x32x16_f16 v[50:65], v[22:25], v[142:145], v[50:65]
	ds_write_b128 v175, v[2:5] offset:32768
	v_cvt_pk_f16_f32 v5, v48, v49
	v_cvt_pk_f16_f32 v4, v46, v47
	v_cvt_pk_f16_f32 v3, v44, v45
	v_cvt_pk_f16_f32 v2, v42, v43
	ds_write_b128 v174, v[2:5] offset:32768
	ds_read_b128 v[2:5], v181
	ds_read_b128 v[6:9], v181 offset:32768
	v_mfma_f32_32x32x16_f16 v[66:81], v[26:29], v[126:129], v[66:81]
	ds_read_b128 v[10:13], v177
	ds_read_b128 v[14:17], v177 offset:32768
	s_waitcnt lgkmcnt(8)
	v_mfma_f32_32x32x16_f16 v[50:65], v[30:33], v[138:141], v[50:65]
	v_mfma_f32_32x32x16_f16 v[66:81], v[22:25], v[122:125], v[66:81]
	s_nop 10
	v_cvt_pk_f16_f32 v57, v56, v57
	v_cvt_pk_f16_f32 v56, v54, v55
	v_cvt_pk_f16_f32 v55, v52, v53
	v_cvt_pk_f16_f32 v54, v50, v51
	v_cvt_pk_f16_f32 v187, v64, v65
	v_cvt_pk_f16_f32 v186, v62, v63
	v_cvt_pk_f16_f32 v185, v60, v61
	v_mfma_f32_32x32x16_f16 v[66:81], v[30:33], v[130:133], v[66:81]
	v_cvt_pk_f16_f32 v184, v58, v59
	v_mfma_f32_32x32x16_f16 v[18:33], v[54:57], v[118:121], 0
	s_nop 9
	v_cvt_pk_f16_f32 v73, v72, v73
	v_cvt_pk_f16_f32 v72, v70, v71
	v_cvt_pk_f16_f32 v71, v68, v69
	v_cvt_pk_f16_f32 v70, v66, v67
	v_cvt_pk_f16_f32 v69, v80, v81
	v_cvt_pk_f16_f32 v68, v78, v79
	v_cvt_pk_f16_f32 v67, v76, v77
	v_mfma_f32_32x32x16_f16 v[50:65], v[54:57], v[102:105], 0
	v_cvt_pk_f16_f32 v66, v74, v75
	v_mfma_f32_32x32x16_f16 v[18:33], v[184:187], v[114:117], v[18:33]
	v_mfma_f32_32x32x16_f16 v[50:65], v[184:187], v[98:101], v[50:65]
	s_waitcnt lgkmcnt(3)
	v_mfma_f32_32x32x16_f16 v[34:49], v[2:5], v[150:153], 0
	v_mfma_f32_32x32x16_f16 v[18:33], v[70:73], v[110:113], v[18:33]
	v_mfma_f32_32x32x16_f16 v[50:65], v[70:73], v[94:97], v[50:65]
	s_waitcnt lgkmcnt(1)
	v_mfma_f32_32x32x16_f16 v[34:49], v[10:13], v[146:149], v[34:49]
	v_mfma_f32_32x32x16_f16 v[18:33], v[66:69], v[106:109], v[18:33]
	v_mfma_f32_32x32x16_f16 v[50:65], v[66:69], v[90:93], v[50:65]
	s_nop 10
	v_cvt_pk_f16_f32 v25, v24, v25
	v_cvt_pk_f16_f32 v24, v22, v23
	v_cvt_pk_f16_f32 v23, v20, v21
	v_cvt_pk_f16_f32 v22, v18, v19
	v_cvt_pk_f16_f32 v21, v32, v33
	v_cvt_pk_f16_f32 v20, v30, v31
	v_cvt_pk_f16_f32 v19, v28, v29
	v_mfma_f32_32x32x16_f16 v[66:81], v[2:5], v[134:137], 0
	v_cvt_pk_f16_f32 v18, v26, v27
	v_cvt_pk_f16_f32 v57, v56, v57
	v_cvt_pk_f16_f32 v56, v54, v55
	v_cvt_pk_f16_f32 v55, v52, v53
	v_cvt_pk_f16_f32 v54, v50, v51
	v_and_b32_e32 v134, 1, v156
	v_mfma_f32_32x32x16_f16 v[34:49], v[6:9], v[142:145], v[34:49]
	v_mfma_f32_32x32x16_f16 v[66:81], v[10:13], v[126:129], v[66:81]
	s_waitcnt lgkmcnt(0)
	v_mfma_f32_32x32x16_f16 v[34:49], v[14:17], v[138:141], v[34:49]
	v_mfma_f32_32x32x16_f16 v[66:81], v[6:9], v[122:125], v[66:81]
	s_nop 10
	v_cvt_pk_f16_f32 v41, v40, v41
	v_cvt_pk_f16_f32 v40, v38, v39
	v_cvt_pk_f16_f32 v39, v36, v37
	v_cvt_pk_f16_f32 v38, v34, v35
	v_cvt_pk_f16_f32 v37, v48, v49
	v_cvt_pk_f16_f32 v36, v46, v47
	v_cvt_pk_f16_f32 v35, v44, v45
	v_mfma_f32_32x32x16_f16 v[66:81], v[14:17], v[130:133], v[66:81]
	v_bitop3_b32 v132, v171, s29, v170 bitop3:0x36
	v_bitop3_b32 v131, s3, v154, v160 bitop3:0x36
	ds_write_b128 v132, v[22:25]
	ds_write_b128 v131, v[18:21]
	v_cvt_pk_f16_f32 v34, v42, v43
	s_or_b32 s3, s2, 0x18e0
	s_or_b32 s2, s2, 0x1ae0
	v_mfma_f32_32x32x16_f16 v[2:17], v[38:41], v[118:121], 0
	s_nop 3
	v_cvt_pk_f16_f32 v45, v72, v73
	v_cvt_pk_f16_f32 v44, v70, v71
	v_cvt_pk_f16_f32 v43, v68, v69
	v_cvt_pk_f16_f32 v42, v66, v67
	v_cvt_pk_f16_f32 v49, v80, v81
	v_cvt_pk_f16_f32 v48, v78, v79
	v_cvt_pk_f16_f32 v47, v76, v77
	v_mfma_f32_32x32x16_f16 v[18:33], v[38:41], v[102:105], 0
	v_cvt_pk_f16_f32 v46, v74, v75
	s_xor_b32 s2, s2, 0x80
	v_cvt_pk_f16_f32 v41, v64, v65
	v_cvt_pk_f16_f32 v40, v62, v63
	v_cvt_pk_f16_f32 v39, v60, v61
	v_cvt_pk_f16_f32 v38, v58, v59
	v_bitop3_b32 v135, v171, s3, v170 bitop3:0x36
	v_mfma_f32_32x32x16_f16 v[2:17], v[34:37], v[114:117], v[2:17]
	v_xor_b32_e32 v133, s2, v154
	ds_write_b128 v132, v[54:57] offset:32768
	ds_write_b128 v131, v[38:41] offset:32768
	v_and_b32_e32 v130, 4, v156
	v_mfma_f32_32x32x16_f16 v[18:33], v[34:37], v[98:101], v[18:33]
	v_mfma_f32_32x32x16_f16 v[2:17], v[42:45], v[110:113], v[2:17]
	v_mfma_f32_32x32x16_f16 v[18:33], v[42:45], v[94:97], v[18:33]
	v_mfma_f32_32x32x16_f16 v[2:17], v[46:49], v[106:109], v[2:17]
	v_mfma_f32_32x32x16_f16 v[18:33], v[46:49], v[90:93], v[18:33]
	s_nop 10
	v_cvt_pk_f16_f32 v9, v8, v9
	v_cvt_pk_f16_f32 v8, v6, v7
	v_cvt_pk_f16_f32 v7, v4, v5
	v_cvt_pk_f16_f32 v6, v2, v3
	v_cvt_pk_f16_f32 v5, v16, v17
	v_cvt_pk_f16_f32 v4, v14, v15
	v_cvt_pk_f16_f32 v3, v12, v13
	v_cvt_pk_f16_f32 v2, v10, v11
	ds_write_b128 v135, v[6:9]
	ds_write_b128 v133, v[2:5]
	v_cvt_pk_f16_f32 v5, v24, v25
	v_cvt_pk_f16_f32 v4, v22, v23
	v_cvt_pk_f16_f32 v3, v20, v21
	v_cvt_pk_f16_f32 v2, v18, v19
	ds_write_b128 v135, v[2:5] offset:32768
	v_cvt_pk_f16_f32 v5, v32, v33
	v_cvt_pk_f16_f32 v4, v30, v31
	v_cvt_pk_f16_f32 v3, v28, v29
	v_cvt_pk_f16_f32 v2, v26, v27
	ds_write_b128 v133, v[2:5] offset:32768
	s_setprio 0
	s_lshl_b32 s2, s27, 3
	s_lshl_b32 s3, s5, 2
	s_or_b32 s2, s3, s2
	s_ashr_i32 s3, s2, 31
	s_lshl_b64 s[2:3], s[2:3], 13
	s_add_u32 s2, s20, s2
	s_addc_u32 s3, s21, s3
	v_lshlrev_b32_e32 v154, 1, v169
	v_lshl_add_u64 v[2:3], s[2:3], 0, v[154:155]
	v_add_co_u32_e32 v2, vcc, s23, v2
	s_waitcnt lgkmcnt(0)
	s_nop 0
	v_addc_co_u32_e32 v3, vcc, 0, v3, vcc
	s_barrier
	global_load_dwordx4 v[62:65], v154, s[2:3]
	global_load_dwordx4 v[46:49], v154, s[2:3] offset:1024
	global_load_dwordx4 v[42:45], v154, s[2:3] offset:2048
	global_load_dwordx4 v[38:41], v154, s[2:3] offset:3072
	global_load_dwordx4 v[54:57], v[2:3], off offset:1024
	global_load_dwordx4 v[50:53], v[2:3], off offset:2048
	v_lshl_add_u64 v[4:5], s[12:13], 0, v[154:155]
	global_load_dwordx4 v[126:129], v154, s[12:13]
	global_load_dwordx4 v[122:125], v154, s[12:13] offset:1024
	global_load_dwordx4 v[118:121], v154, s[12:13] offset:2048
	global_load_dwordx4 v[114:117], v154, s[12:13] offset:3072
	global_load_dwordx4 v[34:37], v168, s[2:3]
	global_load_dwordx4 v[110:113], v168, s[12:13]
	v_add_co_u32_e32 v4, vcc, s23, v4
	s_nop 1
	v_addc_co_u32_e32 v5, vcc, 0, v5, vcc
	global_load_dwordx4 v[58:61], v[2:3], off offset:3072
	global_load_dwordx4 v[106:109], v[4:5], off offset:1024
	global_load_dwordx4 v[94:97], v[4:5], off offset:2048
	global_load_dwordx4 v[90:93], v[4:5], off offset:3072
	v_bfrev_b32_e32 v3, v156
	v_lshlrev_b32_e32 v7, 5, v167
	v_lshlrev_b32_e32 v6, 9, v167
	v_and_b32_e32 v7, 0x200, v7
	v_lshlrev_b32_e32 v8, 8, v167
	v_lshrrev_b32_e32 v3, 27, v3
	v_lshrrev_b32_e32 v2, 2, v167
	v_lshrrev_b32_e32 v4, 4, v156
	v_xor_b32_e32 v5, v169, v156
	v_and_b32_e32 v6, 0x5800, v6
	v_and_b32_e32 v3, 8, v3
	v_and_or_b32 v7, v8, s24, v7
	v_lshrrev_b32_e32 v5, 1, v5
	v_xor_b32_e32 v4, v2, v4
	v_or3_b32 v3, v7, v6, v3
	v_bitop3_b32 v7, v2, v182, 1 bitop3:0x6c
	v_lshlrev_b32_e32 v2, 1, v167
	v_and_b32_e32 v5, 4, v5
	v_lshlrev_b32_e32 v4, 3, v4
	v_lshrrev_b32_e32 v6, 1, v167
	v_and_b32_e32 v2, 2, v2
	v_and_or_b32 v9, v169, 8, v2
	v_and_b32_e32 v2, 8, v4
	v_and_or_b32 v4, v6, 2, v5
	v_or3_b32 v2, v4, v2, v134
	v_lshlrev_b32_e32 v2, 4, v2
	v_bitop3_b32 v146, v3, s28, v2 bitop3:0x36
	v_xor_b32_e32 v8, v6, v182
	v_xor_b32_e32 v147, 0x2010, v146
	ds_read_b64_tr_b16 v[2:3], v146
	ds_read_b64_tr_b16 v[4:5], v147
	v_lshlrev_b32_e32 v8, 2, v8
	v_and_b32_e32 v8, 4, v8
	v_or3_b32 v6, v9, v7, v8
	v_lshlrev_b32_e32 v7, 11, v167
	v_and_b32_e32 v8, 0x7800, v7
	v_lshlrev_b32_e32 v6, 4, v6
	v_or3_b32 v22, v6, v8, v170
	v_and_b32_e32 v23, 0x8000, v7
	s_waitcnt vmcnt(17) lgkmcnt(0)
	v_mfma_f32_32x32x16_f16 v[2:17], v[2:5], v[86:89], 0
	ds_read_b64_tr_b16 v[20:21], v147 offset:32768
	ds_read_b64_tr_b16 v[18:19], v146 offset:32768
	v_xor_b32_e32 v150, 16, v146
	v_xad_u32 v70, v22, s28, v23
	v_xor_b32_e32 v151, 0x2000, v146
	ds_read_b64_tr_b16 v[22:23], v150
	ds_read_b64_tr_b16 v[24:25], v151
	ds_read_b64_tr_b16 v[28:29], v151 offset:32768
	ds_read_b64_tr_b16 v[26:27], v150 offset:32768
	v_xor_b32_e32 v30, 0x280, v70
	v_xor_b32_e32 v148, 32, v146
	s_waitcnt vmcnt(16) lgkmcnt(4)
	v_mfma_f32_32x32x16_f16 v[2:17], v[18:21], v[82:85], v[2:17]
	v_xor_b32_e32 v149, 0x2030, v146
	v_xor_b32_e32 v144, 48, v146
	v_xor_b32_e32 v145, 0x2020, v146
	v_xor_b32_e32 v142, 64, v146
	v_xor_b32_e32 v143, 0x2050, v146
	v_xor_b32_e32 v140, 0x50, v146
	v_xor_b32_e32 v141, 0x2040, v146
	s_nop 4
	v_cvt_pk_f16_f32 v9, v8, v9
	v_cvt_pk_f16_f32 v8, v6, v7
	v_cvt_pk_f16_f32 v7, v4, v5
	v_cvt_pk_f16_f32 v6, v2, v3
	ds_write_b128 v70, v[6:9]
	v_cvt_pk_f16_f32 v21, v16, v17
	v_cvt_pk_f16_f32 v20, v14, v15
	v_cvt_pk_f16_f32 v19, v12, v13
	v_cvt_pk_f16_f32 v18, v10, v11
	s_waitcnt lgkmcnt(3)
	v_mfma_f32_32x32x16_f16 v[2:17], v[22:25], v[86:89], 0
	ds_write_b128 v30, v[18:21]
	ds_read_b64_tr_b16 v[18:19], v148
	ds_read_b64_tr_b16 v[20:21], v149
	ds_read_b64_tr_b16 v[24:25], v149 offset:32768
	ds_read_b64_tr_b16 v[22:23], v148 offset:32768
	v_xor_b32_e32 v30, 0x290, v70
	v_xor_b32_e32 v138, 0x60, v146
	v_xor_b32_e32 v139, 0x2070, v146
	v_xor_b32_e32 v136, 0x70, v146
	v_xor_b32_e32 v137, 0x2060, v146
	s_waitcnt lgkmcnt(6)
	v_mfma_f32_32x32x16_f16 v[2:17], v[26:29], v[82:85], v[2:17]
	v_xor_b32_e32 v26, 16, v70
	v_xor_b32_e32 v71, 0x60, v70
	s_lshl_b64 s[0:1], s[0:1], 13
	s_add_u32 s0, s8, s0
	s_addc_u32 s1, s9, s1
	s_nop 6
	v_cvt_pk_f16_f32 v9, v8, v9
	v_cvt_pk_f16_f32 v8, v6, v7
	v_cvt_pk_f16_f32 v7, v4, v5
	v_cvt_pk_f16_f32 v6, v2, v3
	ds_write_b128 v26, v[6:9]
	v_cvt_pk_f16_f32 v29, v16, v17
	v_cvt_pk_f16_f32 v28, v14, v15
	v_cvt_pk_f16_f32 v27, v12, v13
	v_cvt_pk_f16_f32 v26, v10, v11
	s_waitcnt lgkmcnt(3)
	v_mfma_f32_32x32x16_f16 v[2:17], v[18:21], v[86:89], 0
	ds_write_b128 v30, v[26:29]
	ds_read_b64_tr_b16 v[18:19], v144
	ds_read_b64_tr_b16 v[20:21], v145
	ds_read_b64_tr_b16 v[28:29], v145 offset:32768
	ds_read_b64_tr_b16 v[26:27], v144 offset:32768
	v_xor_b32_e32 v30, 0x2a0, v70
	s_waitcnt lgkmcnt(6)
	v_mfma_f32_32x32x16_f16 v[2:17], v[22:25], v[82:85], v[2:17]
	v_xor_b32_e32 v22, 32, v70
	s_nop 10
	v_cvt_pk_f16_f32 v9, v8, v9
	v_cvt_pk_f16_f32 v8, v6, v7
	v_cvt_pk_f16_f32 v7, v4, v5
	v_cvt_pk_f16_f32 v6, v2, v3
	ds_write_b128 v22, v[6:9]
	v_cvt_pk_f16_f32 v25, v16, v17
	v_cvt_pk_f16_f32 v24, v14, v15
	v_cvt_pk_f16_f32 v23, v12, v13
	v_cvt_pk_f16_f32 v22, v10, v11
	s_waitcnt lgkmcnt(3)
	v_mfma_f32_32x32x16_f16 v[2:17], v[18:21], v[86:89], 0
	ds_write_b128 v30, v[22:25]
	ds_read_b64_tr_b16 v[18:19], v142
	ds_read_b64_tr_b16 v[20:21], v143
	ds_read_b64_tr_b16 v[24:25], v143 offset:32768
	ds_read_b64_tr_b16 v[22:23], v142 offset:32768
	v_xor_b32_e32 v30, 0x2b0, v70
	s_waitcnt lgkmcnt(6)
	v_mfma_f32_32x32x16_f16 v[2:17], v[26:29], v[82:85], v[2:17]
	v_xor_b32_e32 v26, 48, v70
	s_nop 10
	v_cvt_pk_f16_f32 v9, v8, v9
	v_cvt_pk_f16_f32 v8, v6, v7
	v_cvt_pk_f16_f32 v7, v4, v5
	v_cvt_pk_f16_f32 v6, v2, v3
	ds_write_b128 v26, v[6:9]
	v_cvt_pk_f16_f32 v29, v16, v17
	v_cvt_pk_f16_f32 v28, v14, v15
	v_cvt_pk_f16_f32 v27, v12, v13
	v_cvt_pk_f16_f32 v26, v10, v11
	s_waitcnt lgkmcnt(3)
	v_mfma_f32_32x32x16_f16 v[2:17], v[18:21], v[86:89], 0
	ds_write_b128 v30, v[26:29]
	ds_read_b64_tr_b16 v[18:19], v140
	ds_read_b64_tr_b16 v[20:21], v141
	ds_read_b64_tr_b16 v[28:29], v141 offset:32768
	ds_read_b64_tr_b16 v[26:27], v140 offset:32768
	s_waitcnt lgkmcnt(6)
	v_mfma_f32_32x32x16_f16 v[2:17], v[22:25], v[82:85], v[2:17]
	v_xor_b32_e32 v22, 64, v70
	s_nop 10
	v_cvt_pk_f16_f32 v9, v8, v9
	v_cvt_pk_f16_f32 v8, v6, v7
	v_cvt_pk_f16_f32 v7, v4, v5
	v_cvt_pk_f16_f32 v6, v2, v3
	ds_write_b128 v22, v[6:9]
	v_cvt_pk_f16_f32 v5, v16, v17
	v_cvt_pk_f16_f32 v4, v14, v15
	v_cvt_pk_f16_f32 v3, v12, v13
	v_cvt_pk_f16_f32 v2, v10, v11
	s_waitcnt lgkmcnt(3)
	v_mfma_f32_32x32x16_f16 v[10:25], v[18:21], v[86:89], 0
	v_xor_b32_e32 v6, 0x2c0, v70
	ds_write_b128 v6, v[2:5]
	ds_read_b64_tr_b16 v[2:3], v138
	ds_read_b64_tr_b16 v[4:5], v139
	ds_read_b64_tr_b16 v[32:33], v139 offset:32768
	ds_read_b64_tr_b16 v[30:31], v138 offset:32768
	s_waitcnt lgkmcnt(6)
	v_mfma_f32_32x32x16_f16 v[10:25], v[26:29], v[82:85], v[10:25]
	v_xor_b32_e32 v26, 0x50, v70
	s_nop 10
	v_cvt_pk_f16_f32 v9, v16, v17
	v_cvt_pk_f16_f32 v8, v14, v15
	v_cvt_pk_f16_f32 v7, v12, v13
	v_cvt_pk_f16_f32 v6, v10, v11
	ds_write_b128 v26, v[6:9]
	s_waitcnt lgkmcnt(3)
	v_mfma_f32_32x32x16_f16 v[2:17], v[2:5], v[86:89], 0
	v_cvt_pk_f16_f32 v25, v24, v25
	v_cvt_pk_f16_f32 v24, v22, v23
	v_cvt_pk_f16_f32 v23, v20, v21
	v_cvt_pk_f16_f32 v22, v18, v19
	v_xor_b32_e32 v18, 0x2d0, v70
	ds_write_b128 v18, v[22:25]
	ds_read_b64_tr_b16 v[18:19], v136
	ds_read_b64_tr_b16 v[20:21], v137
	s_waitcnt lgkmcnt(4)
	v_mfma_f32_32x32x16_f16 v[2:17], v[30:33], v[82:85], v[2:17]
	ds_read_b64_tr_b16 v[68:69], v137 offset:32768
	ds_read_b64_tr_b16 v[66:67], v136 offset:32768
	s_waitcnt lgkmcnt(2)
	v_mfma_f32_32x32x16_f16 v[18:33], v[18:21], v[86:89], 0
	s_nop 7
	v_cvt_pk_f16_f32 v9, v8, v9
	v_cvt_pk_f16_f32 v8, v6, v7
	v_cvt_pk_f16_f32 v7, v4, v5
	v_cvt_pk_f16_f32 v6, v2, v3
	ds_write_b128 v71, v[6:9]
	v_cvt_pk_f16_f32 v5, v16, v17
	v_cvt_pk_f16_f32 v4, v14, v15
	s_waitcnt lgkmcnt(1)
	v_mfma_f32_32x32x16_f16 v[18:33], v[66:69], v[82:85], v[18:33]
	v_cvt_pk_f16_f32 v3, v12, v13
	v_cvt_pk_f16_f32 v2, v10, v11
	v_xor_b32_e32 v6, 0x2e0, v70
	ds_write_b128 v6, v[2:5]
	v_xor_b32_e32 v6, 0x70, v70
	s_nop 6
	v_cvt_pk_f16_f32 v5, v24, v25
	v_cvt_pk_f16_f32 v4, v22, v23
	v_cvt_pk_f16_f32 v3, v20, v21
	v_cvt_pk_f16_f32 v2, v18, v19
	ds_write_b128 v6, v[2:5]
	v_cvt_pk_f16_f32 v5, v32, v33
	v_cvt_pk_f16_f32 v4, v30, v31
	v_cvt_pk_f16_f32 v3, v28, v29
	v_cvt_pk_f16_f32 v2, v26, v27
	v_xor_b32_e32 v6, 0x2f0, v70
	ds_write_b128 v6, v[2:5]
	v_lshl_add_u64 v[2:3], s[0:1], 0, v[154:155]
	v_lshl_add_u64 v[4:5], v[2:3], 0, s[18:19]
	v_add_co_u32_e32 v2, vcc, s25, v2
	s_waitcnt lgkmcnt(0)
	s_nop 0
	v_addc_co_u32_e32 v3, vcc, 0, v3, vcc
	s_barrier
	global_load_dwordx4 v[102:105], v[2:3], off
	global_load_dwordx4 v[98:101], v[4:5], off offset:1024
	s_setprio 1
	s_add_u32 s0, s2, 0x2000
	s_addc_u32 s1, s3, 0
	v_lshl_add_u64 v[2:3], s[0:1], 0, v[154:155]
	v_add_co_u32_e32 v2, vcc, s23, v2
	global_load_dwordx4 v[66:69], v154, s[0:1]
	global_load_dwordx4 v[70:73], v154, s[0:1] offset:1024
	global_load_dwordx4 v[74:77], v154, s[0:1] offset:2048
	global_load_dwordx4 v[78:81], v154, s[0:1] offset:3072
	v_addc_co_u32_e32 v3, vcc, 0, v3, vcc
	global_load_dwordx4 v[82:85], v168, s[0:1]
	global_load_dwordx4 v[86:89], v[2:3], off offset:1024
	global_load_dwordx4 v[182:185], v[2:3], off offset:2048
	global_load_dwordx4 v[186:189], v[2:3], off offset:3072
	ds_read_b128 v[18:21], v179
	ds_read_b128 v[22:25], v179 offset:32768
	ds_read_b128 v[26:29], v178
	ds_read_b128 v[30:33], v178 offset:32768
	s_add_u32 s0, s2, 0x6000
	s_addc_u32 s1, s3, 0
	s_waitcnt vmcnt(25) lgkmcnt(3)
	v_mfma_f32_32x32x16_f16 v[2:17], v[18:21], v[62:65], 0
	s_add_u32 s2, s2, 0x4000
	s_addc_u32 s3, s3, 0
	s_or_b32 s27, s26, 0x8a0
	s_or_b32 s26, s26, 0xa20
	s_waitcnt vmcnt(24) lgkmcnt(1)
	v_mfma_f32_32x32x16_f16 v[2:17], v[26:29], v[46:49], v[2:17]
	s_waitcnt vmcnt(23)
	v_mfma_f32_32x32x16_f16 v[2:17], v[22:25], v[42:45], v[2:17]
	s_waitcnt vmcnt(22) lgkmcnt(0)
	v_mfma_f32_32x32x16_f16 v[2:17], v[30:33], v[38:41], v[2:17]
	s_waitcnt vmcnt(15)
	v_mfma_f32_32x32x16_f16 v[34:49], v[18:21], v[34:37], 0
	s_nop 9
	v_cvt_pk_f16_f32 v9, v8, v9
	v_cvt_pk_f16_f32 v8, v6, v7
	v_cvt_pk_f16_f32 v7, v4, v5
	v_cvt_pk_f16_f32 v6, v2, v3
	v_cvt_pk_f16_f32 v5, v16, v17
	v_cvt_pk_f16_f32 v4, v14, v15
	v_cvt_pk_f16_f32 v3, v12, v13
	v_mfma_f32_32x32x16_f16 v[34:49], v[26:29], v[54:57], v[34:49]
	v_cvt_pk_f16_f32 v2, v10, v11
	v_mfma_f32_32x32x16_f16 v[34:49], v[22:25], v[50:53], v[34:49]
	s_waitcnt vmcnt(13)
	v_mfma_f32_32x32x16_f16 v[34:49], v[30:33], v[58:61], v[34:49]
	v_mfma_f32_32x32x16_f16 v[18:33], v[6:9], v[126:129], 0
	s_nop 10
	v_cvt_pk_f16_f32 v13, v40, v41
	v_cvt_pk_f16_f32 v12, v38, v39
	v_cvt_pk_f16_f32 v11, v36, v37
	v_cvt_pk_f16_f32 v10, v34, v35
	v_cvt_pk_f16_f32 v17, v48, v49
	v_cvt_pk_f16_f32 v16, v46, v47
	v_cvt_pk_f16_f32 v15, v44, v45
	v_mfma_f32_32x32x16_f16 v[50:65], v[6:9], v[110:113], 0
	v_bitop3_b32 v6, v171, s27, v170 bitop3:0x36
	v_cvt_pk_f16_f32 v14, v42, v43
	v_mfma_f32_32x32x16_f16 v[18:33], v[2:5], v[122:125], v[18:33]
	s_waitcnt vmcnt(12)
	v_mfma_f32_32x32x16_f16 v[50:65], v[2:5], v[106:109], v[50:65]
	ds_read_b128 v[2:5], v6
	ds_read_b128 v[6:9], v6 offset:32768
	v_mfma_f32_32x32x16_f16 v[18:33], v[10:13], v[118:121], v[18:33]
	s_waitcnt vmcnt(11)
	v_mfma_f32_32x32x16_f16 v[50:65], v[10:13], v[94:97], v[50:65]
	s_waitcnt vmcnt(7) lgkmcnt(1)
	v_mfma_f32_32x32x16_f16 v[34:49], v[2:5], v[66:69], 0
	v_mfma_f32_32x32x16_f16 v[18:33], v[14:17], v[114:117], v[18:33]
	v_mfma_f32_32x32x16_f16 v[50:65], v[14:17], v[90:93], v[50:65]
	v_bitop3_b32 v14, v171, s26, v170 bitop3:0x36
	ds_read_b128 v[10:13], v14
	ds_read_b128 v[14:17], v14 offset:32768
	s_nop 7
	v_cvt_pk_f16_f32 v25, v24, v25
	v_cvt_pk_f16_f32 v24, v22, v23
	v_cvt_pk_f16_f32 v23, v20, v21
	v_cvt_pk_f16_f32 v22, v18, v19
	v_cvt_pk_f16_f32 v21, v32, v33
	s_waitcnt vmcnt(6) lgkmcnt(1)
	v_mfma_f32_32x32x16_f16 v[34:49], v[10:13], v[70:73], v[34:49]
	v_cvt_pk_f16_f32 v20, v30, v31
	v_cvt_pk_f16_f32 v19, v28, v29
	v_cvt_pk_f16_f32 v18, v26, v27
	ds_write_b128 v173, v[22:25]
	ds_write_b128 v172, v[18:21]
	v_cvt_pk_f16_f32 v21, v56, v57
	v_cvt_pk_f16_f32 v20, v54, v55
	s_waitcnt vmcnt(5)
	v_mfma_f32_32x32x16_f16 v[34:49], v[6:9], v[74:77], v[34:49]
	v_cvt_pk_f16_f32 v19, v52, v53
	v_cvt_pk_f16_f32 v18, v50, v51
	ds_write_b128 v173, v[18:21] offset:32768
	v_cvt_pk_f16_f32 v21, v64, v65
	v_cvt_pk_f16_f32 v20, v62, v63
	v_cvt_pk_f16_f32 v19, v60, v61
	v_cvt_pk_f16_f32 v18, v58, v59
	s_waitcnt vmcnt(4) lgkmcnt(3)
	v_mfma_f32_32x32x16_f16 v[34:49], v[14:17], v[78:81], v[34:49]
	ds_write_b128 v172, v[18:21] offset:32768
	s_waitcnt vmcnt(3)
	v_mfma_f32_32x32x16_f16 v[66:81], v[2:5], v[82:85], 0
	s_nop 8
	v_cvt_pk_f16_f32 v41, v40, v41
	v_cvt_pk_f16_f32 v40, v38, v39
	v_cvt_pk_f16_f32 v39, v36, v37
	v_cvt_pk_f16_f32 v38, v34, v35
	v_cvt_pk_f16_f32 v85, v48, v49
	v_cvt_pk_f16_f32 v84, v46, v47
	v_cvt_pk_f16_f32 v83, v44, v45
	s_waitcnt vmcnt(2)
	v_mfma_f32_32x32x16_f16 v[66:81], v[10:13], v[86:89], v[66:81]
	v_cvt_pk_f16_f32 v82, v42, v43
	s_waitcnt vmcnt(1)
	v_mfma_f32_32x32x16_f16 v[66:81], v[6:9], v[182:185], v[66:81]
	s_waitcnt vmcnt(0)
	v_mfma_f32_32x32x16_f16 v[66:81], v[14:17], v[186:189], v[66:81]
	v_mfma_f32_32x32x16_f16 v[2:17], v[38:41], v[126:129], 0
	s_nop 10
	v_cvt_pk_f16_f32 v73, v72, v73
	v_cvt_pk_f16_f32 v72, v70, v71
	v_cvt_pk_f16_f32 v70, v66, v67
	v_cvt_pk_f16_f32 v67, v76, v77
	v_cvt_pk_f16_f32 v66, v74, v75
	global_load_dwordx4 v[74:77], v154, s[2:3]
	v_cvt_pk_f16_f32 v71, v68, v69
	v_cvt_pk_f16_f32 v69, v80, v81
	v_cvt_pk_f16_f32 v68, v78, v79
	global_load_dwordx4 v[78:81], v154, s[2:3] offset:1024
	ds_read_b128 v[18:21], v180
	ds_read_b128 v[22:25], v176
	ds_read_b128 v[26:29], v180 offset:32768
	global_load_dwordx4 v[30:33], v154, s[2:3] offset:2048
	v_mfma_f32_32x32x16_f16 v[34:49], v[38:41], v[110:113], 0
	v_mfma_f32_32x32x16_f16 v[2:17], v[82:85], v[122:125], v[2:17]
	v_mfma_f32_32x32x16_f16 v[34:49], v[82:85], v[106:109], v[34:49]
	ds_read_b128 v[82:85], v176 offset:32768
	s_waitcnt vmcnt(2) lgkmcnt(3)
	v_mfma_f32_32x32x16_f16 v[50:65], v[18:21], v[74:77], 0
	v_mfma_f32_32x32x16_f16 v[2:17], v[70:73], v[118:121], v[2:17]
	v_mfma_f32_32x32x16_f16 v[34:49], v[70:73], v[94:97], v[34:49]
	v_lshl_add_u64 v[70:71], s[2:3], 0, v[154:155]
	v_add_co_u32_e32 v152, vcc, s23, v70
	s_nop 1
	v_addc_co_u32_e32 v153, vcc, 0, v71, vcc
	s_waitcnt vmcnt(1) lgkmcnt(2)
	v_mfma_f32_32x32x16_f16 v[50:65], v[22:25], v[78:81], v[50:65]
	v_mfma_f32_32x32x16_f16 v[2:17], v[66:69], v[114:117], v[2:17]
	v_mfma_f32_32x32x16_f16 v[34:49], v[66:69], v[90:93], v[34:49]
	global_load_dwordx4 v[66:69], v154, s[2:3] offset:3072
	s_nop 9
	v_cvt_pk_f16_f32 v9, v8, v9
	v_cvt_pk_f16_f32 v8, v6, v7
	v_cvt_pk_f16_f32 v7, v4, v5
	v_cvt_pk_f16_f32 v6, v2, v3
	v_cvt_pk_f16_f32 v5, v16, v17
	v_cvt_pk_f16_f32 v4, v14, v15
	s_waitcnt vmcnt(1) lgkmcnt(1)
	v_mfma_f32_32x32x16_f16 v[50:65], v[26:29], v[30:33], v[50:65]
	global_load_dwordx4 v[30:33], v168, s[2:3]
	global_load_dwordx4 v[86:89], v[152:153], off offset:1024
	s_nop 0
	global_load_dwordx4 v[168:171], v168, s[0:1]
	v_cvt_pk_f16_f32 v3, v12, v13
	v_cvt_pk_f16_f32 v2, v10, v11
	ds_write_b128 v175, v[6:9]
	ds_write_b128 v174, v[2:5]
	v_cvt_pk_f16_f32 v5, v40, v41
	s_waitcnt vmcnt(3) lgkmcnt(2)
	v_mfma_f32_32x32x16_f16 v[50:65], v[82:85], v[66:69], v[50:65]
	global_load_dwordx4 v[182:185], v154, s[0:1] offset:1024
	v_cvt_pk_f16_f32 v4, v38, v39
	v_cvt_pk_f16_f32 v3, v36, v37
	v_cvt_pk_f16_f32 v2, v34, v35
	ds_write_b128 v175, v[2:5] offset:32768
	v_cvt_pk_f16_f32 v5, v48, v49
	v_cvt_pk_f16_f32 v4, v46, v47
	s_waitcnt vmcnt(3)
	v_mfma_f32_32x32x16_f16 v[66:81], v[18:21], v[30:33], 0
	global_load_dwordx4 v[18:21], v[152:153], off offset:2048
	v_cvt_pk_f16_f32 v3, v44, v45
	v_cvt_pk_f16_f32 v2, v42, v43
	ds_write_b128 v174, v[2:5] offset:32768
	v_cvt_pk_f16_f32 v57, v56, v57
	v_cvt_pk_f16_f32 v56, v54, v55
	v_cvt_pk_f16_f32 v55, v52, v53
	s_waitcnt vmcnt(3)
	v_mfma_f32_32x32x16_f16 v[66:81], v[22:25], v[86:89], v[66:81]
	global_load_dwordx4 v[22:25], v[152:153], off offset:3072
	v_cvt_pk_f16_f32 v54, v50, v51
	s_waitcnt vmcnt(1)
	v_mfma_f32_32x32x16_f16 v[66:81], v[26:29], v[18:21], v[66:81]
	v_lshl_add_u64 v[18:19], s[0:1], 0, v[154:155]
	v_add_co_u32_e32 v152, vcc, s23, v18
	s_nop 1
	v_addc_co_u32_e32 v153, vcc, 0, v19, vcc
	global_load_dwordx4 v[86:89], v[152:153], off offset:1024
	s_waitcnt vmcnt(1)
	v_mfma_f32_32x32x16_f16 v[66:81], v[82:85], v[22:25], v[66:81]
	v_cvt_pk_f16_f32 v85, v64, v65
	v_cvt_pk_f16_f32 v84, v62, v63
	v_cvt_pk_f16_f32 v83, v60, v61
	v_cvt_pk_f16_f32 v82, v58, v59
	v_mfma_f32_32x32x16_f16 v[18:33], v[54:57], v[126:129], 0
	s_nop 6
	v_cvt_pk_f16_f32 v73, v72, v73
	v_cvt_pk_f16_f32 v72, v70, v71
	v_cvt_pk_f16_f32 v70, v66, v67
	v_cvt_pk_f16_f32 v67, v76, v77
	v_cvt_pk_f16_f32 v66, v74, v75
	global_load_dwordx4 v[74:77], v154, s[0:1]
	ds_read_b128 v[2:5], v181
	ds_read_b128 v[6:9], v177
	ds_read_b128 v[10:13], v181 offset:32768
	global_load_dwordx4 v[14:17], v154, s[0:1] offset:2048
	global_load_dwordx4 v[34:37], v154, s[0:1] offset:3072
	v_mfma_f32_32x32x16_f16 v[50:65], v[54:57], v[110:113], 0
	v_cvt_pk_f16_f32 v71, v68, v69
	v_cvt_pk_f16_f32 v69, v80, v81
	v_cvt_pk_f16_f32 v68, v78, v79
	v_mfma_f32_32x32x16_f16 v[18:33], v[82:85], v[122:125], v[18:33]
	v_mfma_f32_32x32x16_f16 v[50:65], v[82:85], v[106:109], v[50:65]
	ds_read_b128 v[82:85], v177 offset:32768
	v_mfma_f32_32x32x16_f16 v[18:33], v[70:73], v[118:121], v[18:33]
	v_mfma_f32_32x32x16_f16 v[50:65], v[70:73], v[94:97], v[50:65]
	v_mfma_f32_32x32x16_f16 v[18:33], v[66:69], v[114:117], v[18:33]
	v_mfma_f32_32x32x16_f16 v[50:65], v[66:69], v[90:93], v[50:65]
	s_nop 10
	v_cvt_pk_f16_f32 v25, v24, v25
	v_cvt_pk_f16_f32 v24, v22, v23
	v_cvt_pk_f16_f32 v23, v20, v21
	v_cvt_pk_f16_f32 v22, v18, v19
	ds_write_b128 v132, v[22:25]
	s_waitcnt vmcnt(2) lgkmcnt(4)
	v_mfma_f32_32x32x16_f16 v[66:81], v[2:5], v[74:77], 0
	s_waitcnt lgkmcnt(3)
	v_mfma_f32_32x32x16_f16 v[66:81], v[6:9], v[182:185], v[66:81]
	s_waitcnt vmcnt(1) lgkmcnt(2)
	v_mfma_f32_32x32x16_f16 v[66:81], v[10:13], v[14:17], v[66:81]
	s_waitcnt vmcnt(0) lgkmcnt(1)
	v_mfma_f32_32x32x16_f16 v[66:81], v[82:85], v[34:37], v[66:81]
	v_mfma_f32_32x32x16_f16 v[34:49], v[2:5], v[168:171], 0
	global_load_dwordx4 v[2:5], v[152:153], off offset:2048
	s_nop 9
	v_cvt_pk_f16_f32 v73, v72, v73
	v_cvt_pk_f16_f32 v72, v70, v71
	v_cvt_pk_f16_f32 v71, v68, v69
	v_cvt_pk_f16_f32 v70, v66, v67
	v_cvt_pk_f16_f32 v69, v80, v81
	v_cvt_pk_f16_f32 v68, v78, v79
	v_mfma_f32_32x32x16_f16 v[34:49], v[6:9], v[86:89], v[34:49]
	global_load_dwordx4 v[6:9], v[152:153], off offset:3072
	v_cvt_pk_f16_f32 v67, v76, v77
	v_cvt_pk_f16_f32 v66, v74, v75
	s_waitcnt vmcnt(1)
	v_mfma_f32_32x32x16_f16 v[34:49], v[10:13], v[2:5], v[34:49]
	s_waitcnt vmcnt(0)
	v_mfma_f32_32x32x16_f16 v[34:49], v[82:85], v[6:9], v[34:49]
	v_mfma_f32_32x32x16_f16 v[2:17], v[70:73], v[126:129], 0
	s_nop 10
	v_cvt_pk_f16_f32 v41, v40, v41
	v_cvt_pk_f16_f32 v40, v38, v39
	v_cvt_pk_f16_f32 v38, v34, v35
	v_cvt_pk_f16_f32 v35, v44, v45
	v_cvt_pk_f16_f32 v34, v42, v43
	v_cvt_pk_f16_f32 v45, v32, v33
	v_cvt_pk_f16_f32 v44, v30, v31
	v_cvt_pk_f16_f32 v43, v28, v29
	v_cvt_pk_f16_f32 v42, v26, v27
	v_mfma_f32_32x32x16_f16 v[18:33], v[70:73], v[110:113], 0
	v_cvt_pk_f16_f32 v39, v36, v37
	v_cvt_pk_f16_f32 v37, v48, v49
	v_cvt_pk_f16_f32 v36, v46, v47
	ds_write_b128 v131, v[42:45]
	v_cvt_pk_f16_f32 v45, v56, v57
	v_cvt_pk_f16_f32 v44, v54, v55
	v_cvt_pk_f16_f32 v43, v52, v53
	v_mfma_f32_32x32x16_f16 v[2:17], v[66:69], v[122:125], v[2:17]
	v_cvt_pk_f16_f32 v42, v50, v51
	ds_write_b128 v132, v[42:45] offset:32768
	v_cvt_pk_f16_f32 v45, v64, v65
	v_cvt_pk_f16_f32 v44, v62, v63
	v_cvt_pk_f16_f32 v43, v60, v61
	v_cvt_pk_f16_f32 v42, v58, v59
	ds_write_b128 v131, v[42:45] offset:32768
	v_mfma_f32_32x32x16_f16 v[18:33], v[66:69], v[106:109], v[18:33]
	v_mfma_f32_32x32x16_f16 v[2:17], v[38:41], v[118:121], v[2:17]
	v_mfma_f32_32x32x16_f16 v[18:33], v[38:41], v[94:97], v[18:33]
	v_mfma_f32_32x32x16_f16 v[2:17], v[34:37], v[114:117], v[2:17]
	v_mfma_f32_32x32x16_f16 v[18:33], v[34:37], v[90:93], v[18:33]
	s_nop 10
	v_cvt_pk_f16_f32 v9, v8, v9
	v_cvt_pk_f16_f32 v8, v6, v7
	v_cvt_pk_f16_f32 v7, v4, v5
	v_cvt_pk_f16_f32 v6, v2, v3
	v_cvt_pk_f16_f32 v5, v16, v17
	v_cvt_pk_f16_f32 v4, v14, v15
	v_cvt_pk_f16_f32 v3, v12, v13
	v_cvt_pk_f16_f32 v2, v10, v11
	ds_write_b128 v135, v[6:9]
	ds_write_b128 v133, v[2:5]
	v_cvt_pk_f16_f32 v5, v24, v25
	v_cvt_pk_f16_f32 v4, v22, v23
	v_cvt_pk_f16_f32 v3, v20, v21
	v_cvt_pk_f16_f32 v2, v18, v19
	ds_write_b128 v135, v[2:5] offset:32768
	v_cvt_pk_f16_f32 v5, v32, v33
	v_cvt_pk_f16_f32 v4, v30, v31
	v_cvt_pk_f16_f32 v3, v28, v29
	v_cvt_pk_f16_f32 v2, v26, v27
	ds_write_b128 v133, v[2:5] offset:32768
	s_setprio 0
	s_waitcnt lgkmcnt(0)
	s_barrier
	ds_read_b64_tr_b16 v[2:3], v146
	ds_read_b64_tr_b16 v[4:5], v147
	ds_read_b64_tr_b16 v[36:37], v147 offset:32768
	ds_read_b64_tr_b16 v[34:35], v146 offset:32768
	ds_read_b64_tr_b16 v[18:19], v150
	ds_read_b64_tr_b16 v[20:21], v151
	ds_read_b64_tr_b16 v[40:41], v151 offset:32768
	ds_read_b64_tr_b16 v[38:39], v150 offset:32768
	s_waitcnt lgkmcnt(6)
	v_mfma_f32_32x32x16_f16 v[2:17], v[2:5], v[102:105], 0
	ds_read_b64_tr_b16 v[42:43], v148
	ds_read_b64_tr_b16 v[44:45], v149
	ds_read_b64_tr_b16 v[48:49], v149 offset:32768
	ds_read_b64_tr_b16 v[46:47], v148 offset:32768
	v_cmp_gt_u32_e64 s[0:1], 32, v167
	s_cmp_eq_u32 s5, 0
	v_cmp_lt_i32_e64 s[2:3], v162, v163
	s_waitcnt lgkmcnt(6)
	v_mfma_f32_32x32x16_f16 v[18:33], v[18:21], v[102:105], 0
	v_mfma_f32_32x32x16_f16 v[2:17], v[34:37], v[98:101], v[2:17]
	s_waitcnt lgkmcnt(4)
	v_mfma_f32_32x32x16_f16 v[18:33], v[38:41], v[98:101], v[18:33]
	s_nop 9
	v_mul_f32_e64 v34, v16, v16
	v_mul_f32_e64 v35, v17, v17
	v_mul_f32_e64 v36, v12, v12
	v_mul_f32_e64 v37, v13, v13
	v_mul_f32_e64 v50, v8, v8
	v_mul_f32_e64 v51, v9, v9
	v_pk_mul_f32 v[52:53], v[4:5], v[4:5]
	v_pk_fma_f32 v[50:51], v[6:7], v[6:7], v[50:51]
	v_pk_fma_f32 v[52:53], v[2:3], v[2:3], v[52:53]
	v_pk_fma_f32 v[36:37], v[10:11], v[10:11], v[36:37]
	v_pk_fma_f32 v[34:35], v[14:15], v[14:15], v[34:35]
	v_pk_mul_f32 v[116:117], v[24:25], v[24:25]
	v_pk_mul_f32 v[118:119], v[20:21], v[20:21]
	v_pk_add_f32 v[50:51], v[52:53], v[50:51]
	v_pk_add_f32 v[34:35], v[36:37], v[34:35]
	v_pk_mul_f32 v[112:113], v[32:33], v[32:33]
	v_pk_mul_f32 v[114:115], v[28:29], v[28:29]
	v_pk_mul_f32 v[120:121], v[18:19], v[18:19]
	v_pk_fma_f32 v[18:19], v[18:19], v[18:19], v[118:119]
	v_pk_fma_f32 v[20:21], v[22:23], v[22:23], v[116:117]
	v_pk_add_f32 v[34:35], v[50:51], v[34:35]
	v_pk_mul_f32 v[106:107], v[22:23], v[22:23]
	v_pk_add_f32 v[18:19], v[18:19], v[20:21]
	v_pk_fma_f32 v[20:21], v[26:27], v[26:27], v[114:115]
	v_pk_fma_f32 v[22:23], v[30:31], v[30:31], v[112:113]
	v_add_f32_e32 v34, v34, v35
	v_pk_add_f32 v[20:21], v[20:21], v[22:23]
	v_add_f32_e32 v36, 0, v34
	v_pk_mul_f32 v[108:109], v[26:27], v[26:27]
	v_pk_mul_f32 v[110:111], v[30:31], v[30:31]
	v_pk_add_f32 v[34:35], v[18:19], v[20:21]
	s_waitcnt lgkmcnt(2)
	v_mfma_f32_32x32x16_f16 v[18:33], v[42:45], v[102:105], 0
	v_add_f32_e32 v34, v34, v35
	v_add_f32_e32 v54, v36, v34
	v_sub_f32_e32 v55, v36, v34
	ds_read_b64_tr_b16 v[34:35], v144
	ds_read_b64_tr_b16 v[36:37], v145
	ds_read_b64_tr_b16 v[52:53], v145 offset:32768
	ds_read_b64_tr_b16 v[50:51], v144 offset:32768
	v_pk_fma_f32 v[4:5], v[4:5], v[4:5], v[118:119]
	v_pk_fma_f32 v[16:17], v[16:17], v[16:17], v[112:113]
	v_pk_fma_f32 v[14:15], v[14:15], v[14:15], v[110:111]
	s_waitcnt lgkmcnt(4)
	v_mfma_f32_32x32x16_f16 v[18:33], v[46:49], v[98:101], v[18:33]
	v_fma_f32 v12, v12, v12, v114
	v_fma_f32 v13, v13, v13, v115
	v_fma_f32 v10, v10, v10, v108
	v_fma_f32 v11, v11, v11, v109
	v_fma_f32 v8, v8, v8, v116
	v_fma_f32 v9, v9, v9, v117
	v_pk_fma_f32 v[6:7], v[6:7], v[6:7], v[106:107]
	v_pk_fma_f32 v[2:3], v[2:3], v[2:3], v[120:121]
	s_nop 3
	v_pk_mul_f32 v[38:39], v[32:33], v[32:33]
	v_pk_mul_f32 v[40:41], v[28:29], v[28:29]
	v_pk_mul_f32 v[42:43], v[24:25], v[24:25]
	v_pk_mul_f32 v[44:45], v[20:21], v[20:21]
	v_pk_fma_f32 v[42:43], v[22:23], v[22:23], v[42:43]
	v_pk_fma_f32 v[44:45], v[18:19], v[18:19], v[44:45]
	v_pk_fma_f32 v[40:41], v[26:27], v[26:27], v[40:41]
	v_pk_fma_f32 v[38:39], v[30:31], v[30:31], v[38:39]
	v_pk_add_f32 v[42:43], v[44:45], v[42:43]
	v_pk_add_f32 v[38:39], v[40:41], v[38:39]
	v_pk_fma_f32 v[4:5], v[20:21], v[20:21], v[4:5]
	v_pk_add_f32 v[38:39], v[42:43], v[38:39]
	v_pk_fma_f32 v[6:7], v[22:23], v[22:23], v[6:7]
	v_add_f32_e32 v56, v38, v39
	s_waitcnt lgkmcnt(2)
	v_mfma_f32_32x32x16_f16 v[34:49], v[34:37], v[102:105], 0
	v_add_f32_e32 v70, v54, v56
	v_add_f32_e32 v71, v55, v56
	v_sub_f32_e32 v72, v54, v56
	ds_read_b64_tr_b16 v[54:55], v142
	ds_read_b64_tr_b16 v[56:57], v143
	ds_read_b64_tr_b16 v[68:69], v143 offset:32768
	ds_read_b64_tr_b16 v[66:67], v142 offset:32768
	v_pk_fma_f32 v[8:9], v[24:25], v[24:25], v[8:9]
	v_pk_fma_f32 v[10:11], v[26:27], v[26:27], v[10:11]
	v_pk_fma_f32 v[12:13], v[28:29], v[28:29], v[12:13]
	s_waitcnt lgkmcnt(4)
	v_mfma_f32_32x32x16_f16 v[34:49], v[50:53], v[98:101], v[34:49]
	v_fma_f32 v14, v30, v30, v14
	v_fma_f32 v15, v31, v31, v15
	v_fma_f32 v16, v32, v32, v16
	v_fma_f32 v17, v33, v33, v17
	v_fma_f32 v2, v18, v18, v2
	v_fma_f32 v3, v19, v19, v3
	s_nop 5
	v_pk_mul_f32 v[50:51], v[48:49], v[48:49]
	v_pk_mul_f32 v[52:53], v[44:45], v[44:45]
	v_pk_mul_f32 v[58:59], v[40:41], v[40:41]
	v_pk_mul_f32 v[60:61], v[36:37], v[36:37]
	v_pk_fma_f32 v[58:59], v[38:39], v[38:39], v[58:59]
	v_pk_fma_f32 v[60:61], v[34:35], v[34:35], v[60:61]
	v_pk_fma_f32 v[52:53], v[42:43], v[42:43], v[52:53]
	v_pk_fma_f32 v[50:51], v[46:47], v[46:47], v[50:51]
	v_pk_add_f32 v[58:59], v[60:61], v[58:59]
	v_pk_add_f32 v[50:51], v[52:53], v[50:51]
	v_pk_fma_f32 v[4:5], v[36:37], v[36:37], v[4:5]
	v_pk_add_f32 v[50:51], v[58:59], v[50:51]
	v_pk_fma_f32 v[16:17], v[48:49], v[48:49], v[16:17]
	v_add_f32_e32 v73, v50, v51
	s_waitcnt lgkmcnt(2)
	v_mfma_f32_32x32x16_f16 v[50:65], v[54:57], v[102:105], 0
	v_add_f32_e32 v86, v70, v73
	v_sub_f32_e32 v87, v71, v73
	v_sub_f32_e32 v88, v72, v73
	ds_read_b64_tr_b16 v[70:71], v140
	ds_read_b64_tr_b16 v[72:73], v141
	ds_read_b64_tr_b16 v[84:85], v141 offset:32768
	ds_read_b64_tr_b16 v[82:83], v140 offset:32768
	v_pk_fma_f32 v[14:15], v[46:47], v[46:47], v[14:15]
	v_pk_fma_f32 v[12:13], v[44:45], v[44:45], v[12:13]
	v_pk_fma_f32 v[10:11], v[42:43], v[42:43], v[10:11]
	s_waitcnt lgkmcnt(4)
	v_mfma_f32_32x32x16_f16 v[50:65], v[66:69], v[98:101], v[50:65]
	v_fma_f32 v8, v40, v40, v8
	v_fma_f32 v9, v41, v41, v9
	v_fma_f32 v6, v38, v38, v6
	v_fma_f32 v7, v39, v39, v7
	v_fma_f32 v2, v34, v34, v2
	v_fma_f32 v3, v35, v35, v3
	s_nop 5
	v_pk_mul_f32 v[66:67], v[64:65], v[64:65]
	v_pk_mul_f32 v[68:69], v[60:61], v[60:61]
	v_pk_mul_f32 v[74:75], v[56:57], v[56:57]
	v_pk_mul_f32 v[76:77], v[52:53], v[52:53]
	v_pk_fma_f32 v[74:75], v[54:55], v[54:55], v[74:75]
	v_pk_fma_f32 v[76:77], v[50:51], v[50:51], v[76:77]
	v_pk_fma_f32 v[68:69], v[58:59], v[58:59], v[68:69]
	v_pk_fma_f32 v[66:67], v[62:63], v[62:63], v[66:67]
	v_pk_add_f32 v[74:75], v[76:77], v[74:75]
	v_pk_add_f32 v[66:67], v[68:69], v[66:67]
	v_pk_fma_f32 v[4:5], v[52:53], v[52:53], v[4:5]
	v_pk_add_f32 v[66:67], v[74:75], v[66:67]
	v_pk_fma_f32 v[6:7], v[54:55], v[54:55], v[6:7]
	v_add_f32_e32 v89, v66, v67
	s_waitcnt lgkmcnt(2)
	v_mfma_f32_32x32x16_f16 v[66:81], v[70:73], v[102:105], 0
	v_add_f32_e32 v94, v86, v89
	v_add_f32_e32 v126, v87, v89
	v_add_f32_e32 v127, v88, v89
	v_sub_f32_e32 v128, v86, v89
	ds_read_b64_tr_b16 v[86:87], v138
	ds_read_b64_tr_b16 v[88:89], v139
	ds_read_b64_tr_b16 v[124:125], v139 offset:32768
	ds_read_b64_tr_b16 v[122:123], v138 offset:32768
	v_pk_fma_f32 v[8:9], v[56:57], v[56:57], v[8:9]
	v_pk_fma_f32 v[10:11], v[58:59], v[58:59], v[10:11]
	s_waitcnt lgkmcnt(4)
	v_mfma_f32_32x32x16_f16 v[66:81], v[82:85], v[98:101], v[66:81]
	v_fma_f32 v12, v60, v60, v12
	v_fma_f32 v13, v61, v61, v13
	v_fma_f32 v14, v62, v62, v14
	v_fma_f32 v15, v63, v63, v15
	v_fma_f32 v16, v64, v64, v16
	v_fma_f32 v17, v65, v65, v17
	v_pk_fma_f32 v[2:3], v[50:51], v[50:51], v[2:3]
	s_nop 4
	v_pk_mul_f32 v[82:83], v[80:81], v[80:81]
	v_pk_mul_f32 v[84:85], v[76:77], v[76:77]
	v_pk_mul_f32 v[90:91], v[72:73], v[72:73]
	v_pk_mul_f32 v[92:93], v[68:69], v[68:69]
	v_pk_fma_f32 v[90:91], v[70:71], v[70:71], v[90:91]
	v_pk_fma_f32 v[92:93], v[66:67], v[66:67], v[92:93]
	v_pk_fma_f32 v[84:85], v[74:75], v[74:75], v[84:85]
	v_pk_fma_f32 v[82:83], v[78:79], v[78:79], v[82:83]
	v_pk_add_f32 v[90:91], v[92:93], v[90:91]
	v_pk_add_f32 v[82:83], v[84:85], v[82:83]
	v_pk_fma_f32 v[4:5], v[68:69], v[68:69], v[4:5]
	v_pk_add_f32 v[82:83], v[90:91], v[82:83]
	v_pk_fma_f32 v[18:19], v[80:81], v[80:81], v[16:17]
	v_add_f32_e32 v129, v82, v83
	v_add_f32_e32 v131, v94, v129
	s_waitcnt lgkmcnt(2)
	v_mfma_f32_32x32x16_f16 v[82:97], v[86:89], v[102:105], 0
	v_sub_f32_e32 v135, v126, v129
	v_add_f32_e32 v142, v127, v129
	v_sub_f32_e32 v143, v128, v129
	ds_read_b64_tr_b16 v[126:127], v136
	ds_read_b64_tr_b16 v[128:129], v137
	ds_read_b64_tr_b16 v[138:139], v137 offset:32768
	ds_read_b64_tr_b16 v[136:137], v136 offset:32768
	v_pk_fma_f32 v[20:21], v[78:79], v[78:79], v[14:15]
	v_pk_fma_f32 v[22:23], v[76:77], v[76:77], v[12:13]
	v_pk_fma_f32 v[24:25], v[74:75], v[74:75], v[10:11]
	s_waitcnt lgkmcnt(4)
	v_mfma_f32_32x32x16_f16 v[82:97], v[122:125], v[98:101], v[82:97]
	v_fma_f32 v26, v72, v72, v8
	v_fma_f32 v27, v73, v73, v9
	v_fma_f32 v28, v70, v70, v6
	v_fma_f32 v29, v71, v71, v7
	v_fma_f32 v30, v66, v66, v2
	v_fma_f32 v31, v67, v67, v3
	s_nop 5
	v_pk_fma_f32 v[32:33], v[84:85], v[84:85], v[4:5]
	s_waitcnt lgkmcnt(2)
	v_mfma_f32_32x32x16_f16 v[2:17], v[126:129], v[102:105], 0
	v_fma_f32 v28, v86, v86, v28
	v_fma_f32 v29, v87, v87, v29
	v_fma_f32 v24, v90, v90, v24
	v_fma_f32 v25, v91, v91, v25
	v_fma_f32 v22, v92, v92, v22
	v_fma_f32 v23, v93, v93, v23
	v_pk_fma_f32 v[20:21], v[94:95], v[94:95], v[20:21]
	v_pk_fma_f32 v[18:19], v[96:97], v[96:97], v[18:19]
	v_pk_fma_f32 v[30:31], v[82:83], v[82:83], v[30:31]
	v_pk_fma_f32 v[26:27], v[88:89], v[88:89], v[26:27]
	s_waitcnt lgkmcnt(0)
	v_mfma_f32_32x32x16_f16 v[2:17], v[136:139], v[98:101], v[2:17]
	v_mul_f32_e64 v122, v96, v96
	v_mul_f32_e64 v123, v97, v97
	v_mul_f32_e64 v124, v92, v92
	v_mul_f32_e64 v125, v93, v93
	v_mul_f32_e64 v132, v88, v88
	v_mul_f32_e64 v133, v89, v89
	v_pk_mul_f32 v[140:141], v[84:85], v[84:85]
	v_pk_fma_f32 v[132:133], v[86:87], v[86:87], v[132:133]
	v_pk_fma_f32 v[140:141], v[82:83], v[82:83], v[140:141]
	v_pk_fma_f32 v[124:125], v[90:91], v[90:91], v[124:125]
	s_nop 1
	v_pk_mul_f32 v[38:39], v[8:9], v[8:9]
	v_pk_mul_f32 v[40:41], v[4:5], v[4:5]
	v_pk_mul_f32 v[34:35], v[16:17], v[16:17]
	v_pk_mul_f32 v[36:37], v[12:13], v[12:13]
	v_pk_fma_f32 v[16:17], v[16:17], v[16:17], v[18:19]
	v_pk_fma_f32 v[18:19], v[14:15], v[14:15], v[20:21]
	v_pk_fma_f32 v[12:13], v[12:13], v[12:13], v[22:23]
	v_pk_fma_f32 v[20:21], v[10:11], v[10:11], v[24:25]
	v_pk_fma_f32 v[22:23], v[6:7], v[6:7], v[28:29]
	v_pk_fma_f32 v[24:25], v[2:3], v[2:3], v[30:31]
	v_pk_fma_f32 v[2:3], v[2:3], v[2:3], v[40:41]
	v_pk_fma_f32 v[6:7], v[6:7], v[6:7], v[38:39]
	v_pk_fma_f32 v[4:5], v[4:5], v[4:5], v[32:33]
	v_pk_add_f32 v[2:3], v[2:3], v[6:7]
	v_pk_fma_f32 v[6:7], v[10:11], v[10:11], v[36:37]
	v_pk_fma_f32 v[10:11], v[14:15], v[14:15], v[34:35]
	v_pk_fma_f32 v[8:9], v[8:9], v[8:9], v[26:27]
	v_pk_add_f32 v[6:7], v[6:7], v[10:11]
	v_sub_f32_e32 v10, v24, v25
	v_add_f32_e32 v11, v25, v24
	v_add_f32_e32 v10, v4, v10
	v_sub_f32_e32 v14, v11, v4
	v_add_f32_e32 v4, v4, v11
	v_sub_f32_e32 v10, v10, v5
	v_sub_f32_e32 v11, v14, v5
	v_add_f32_e32 v4, v5, v4
	v_add_f32_e32 v5, v22, v10
	v_add_f32_e32 v10, v22, v11
	v_sub_f32_e32 v11, v4, v22
	v_add_f32_e32 v4, v22, v4
	v_sub_f32_e32 v5, v5, v23
	v_add_f32_e32 v10, v23, v10
	v_sub_f32_e32 v11, v11, v23
	v_add_f32_e32 v4, v23, v4
	v_add_f32_e32 v5, v8, v5
	v_sub_f32_e32 v10, v10, v8
	v_sub_f32_e32 v11, v11, v8
	v_add_f32_e32 v4, v8, v4
	v_sub_f32_e32 v5, v5, v9
	v_pk_fma_f32 v[122:123], v[94:95], v[94:95], v[122:123]
	v_sub_f32_e32 v8, v10, v9
	v_sub_f32_e32 v10, v11, v9
	v_add_f32_e32 v4, v9, v4
	v_add_f32_e32 v5, v20, v5
	v_pk_add_f32 v[132:133], v[140:141], v[132:133]
	v_pk_add_f32 v[122:123], v[124:125], v[122:123]
	v_add_f32_e32 v8, v20, v8
	v_add_f32_e32 v9, v20, v10
	v_sub_f32_e32 v4, v4, v20
	v_sub_f32_e32 v5, v5, v21
	v_pk_add_f32 v[122:123], v[132:133], v[122:123]
	v_add_f32_e32 v8, v21, v8
	v_add_f32_e32 v9, v21, v9
	v_sub_f32_e32 v4, v4, v21
	v_add_f32_e32 v5, v12, v5
	v_add_f32_e32 v122, v122, v123
	v_pk_add_f32 v[2:3], v[2:3], v[6:7]
	v_sub_f32_e32 v8, v8, v12
	v_add_f32_e32 v9, v12, v9
	v_sub_f32_e32 v4, v4, v12
	v_sub_f32_e32 v5, v5, v13
	v_add_f32_e32 v123, v131, v122
	v_add_f32_e32 v2, v2, v3
	v_sub_f32_e32 v8, v8, v13
	v_add_f32_e32 v9, v13, v9
	v_sub_f32_e32 v4, v4, v13
	v_add_f32_e32 v5, v18, v5
	v_add_f32_e32 v3, v123, v2
	v_add_f32_e32 v8, v18, v8
	v_sub_f32_e32 v9, v9, v18
	v_sub_f32_e32 v4, v4, v18
	v_sub_f32_e32 v5, v5, v19
	v_and_b32_e32 v10, 8, v156
	v_add_f32_e32 v8, v19, v8
	v_sub_f32_e32 v9, v9, v19
	v_sub_f32_e32 v4, v4, v19
	v_add_f32_e32 v5, v16, v5
	v_cmp_eq_u32_e32 vcc, 0, v10
	v_cndmask_b32_e64 v10, -v3, v3, s[0:1]
	s_cselect_b64 s[0:1], -1, 0
	s_bitcmp0_b32 s4, 7
	v_sub_f32_e32 v8, v8, v16
	v_sub_f32_e32 v9, v9, v16
	v_sub_f32_e32 v4, v4, v16
	v_sub_f32_e32 v5, v5, v17
	v_cndmask_b32_e64 v11, -v3, v3, s[0:1]
	s_cselect_b64 s[0:1], -1, 0
	v_and_b32_e32 v16, 32, v156
	v_sub_f32_e32 v8, v8, v17
	v_cndmask_b32_e64 v5, -v5, v5, vcc
	v_cndmask_b32_e64 v12, -v3, v3, s[0:1]
	v_cndmask_b32_e64 v18, v161, v162, s[2:3]
	v_cmp_eq_u32_e64 s[2:3], 0, v16
	v_lshlrev_b32_e32 v18, 2, v18
	v_cmp_eq_u32_e64 s[0:1], 0, v134
	v_cndmask_b32_e64 v16, v11, v5, s[2:3]
	v_cndmask_b32_e64 v5, v5, v11, s[2:3]
	v_cndmask_b32_e64 v11, v8, v12, s[2:3]
	ds_bpermute_b32 v11, v18, v11
	v_and_b32_e32 v14, 2, v156
	v_cndmask_b32_e64 v13, -v3, v3, s[0:1]
	v_cmp_eq_u32_e64 s[0:1], 0, v14
	v_cndmask_b32_e64 v8, v12, v8, s[2:3]
	v_add_f32_e32 v124, v135, v122
	v_cndmask_b32_e64 v14, -v3, v3, s[0:1]
	v_cmp_eq_u32_e64 s[0:1], 0, v130
	v_sub_f32_e32 v4, v4, v17
	s_waitcnt lgkmcnt(0)
	v_add_f32_e32 v8, v8, v11
	v_cndmask_b32_e64 v15, -v3, v3, s[0:1]
	v_cndmask_b32_e64 v11, v14, v10, s[2:3]
	v_cndmask_b32_e64 v10, v10, v14, s[2:3]
	v_sub_f32_e32 v6, v124, v2
	v_sub_f32_e32 v9, v9, v17
	v_cndmask_b32_e64 v3, -v3, v3, vcc
	ds_bpermute_b32 v10, v18, v10
	v_cndmask_b32_e64 v12, v4, v15, s[2:3]
	v_sub_f32_e32 v125, v142, v122
	v_cndmask_b32_e64 v19, v9, v13, s[2:3]
	v_cndmask_b32_e64 v9, v13, v9, s[2:3]
	ds_bpermute_b32 v12, v18, v12
	v_cndmask_b32_e64 v13, v6, v3, s[2:3]
	v_sub_f32_e32 v7, v125, v2
	v_bfe_i32 v17, v156, 5, 1
	ds_bpermute_b32 v5, v18, v5
	ds_bpermute_b32 v13, v18, v13
	v_sub_f32_e32 v122, v143, v122
	v_cndmask_b32_e64 v3, v3, v6, s[2:3]
	v_and_b32_e32 v6, v17, v7
	v_sub_f32_e32 v2, v122, v2
	ds_bpermute_b32 v19, v18, v19
	ds_bpermute_b32 v6, v18, v6
	s_waitcnt lgkmcnt(5)
	v_add_f32_e32 v10, v11, v10
	v_cndmask_b32_e64 v4, v15, v4, s[2:3]
	v_and_b32_e32 v11, v17, v2
	s_waitcnt lgkmcnt(4)
	v_add_f32_e32 v4, v4, v12
	ds_bpermute_b32 v11, v18, v11
	v_and_b32_e32 v12, 16, v156
	v_cmp_lt_i32_e64 s[4:5], v164, v163
	s_waitcnt lgkmcnt(4)
	v_add_f32_e32 v5, v16, v5
	s_waitcnt lgkmcnt(3)
	v_add_f32_e32 v3, v3, v13
	v_cndmask_b32_e64 v13, v161, v164, s[4:5]
	v_cmp_eq_u32_e64 s[4:5], 0, v12
	s_waitcnt lgkmcnt(2)
	v_add_f32_e32 v9, v9, v19
	v_lshlrev_b32_e32 v13, 2, v13
	v_cndmask_b32_e64 v12, v4, v5, s[4:5]
	v_cndmask_b32_e64 v4, v5, v4, s[4:5]
	v_cndmask_b32_e64 v5, 0, v7, s[2:3]
	s_waitcnt lgkmcnt(1)
	v_add_f32_e32 v5, v5, v6
	v_cndmask_b32_e64 v2, 0, v2, s[2:3]
	v_cndmask_b32_e64 v7, v9, v5, s[4:5]
	ds_bpermute_b32 v4, v13, v4
	s_waitcnt lgkmcnt(1)
	v_add_f32_e32 v2, v2, v11
	v_cndmask_b32_e64 v6, v3, v8, s[4:5]
	v_cndmask_b32_e64 v3, v8, v3, s[4:5]
	ds_bpermute_b32 v7, v13, v7
	ds_bpermute_b32 v3, v13, v3
	v_cndmask_b32_e64 v8, v10, v2, s[4:5]
	ds_bpermute_b32 v8, v13, v8
	v_cndmask_b32_e64 v5, v5, v9, s[4:5]
	s_waitcnt lgkmcnt(3)
	v_add_f32_e32 v4, v12, v4
	s_waitcnt lgkmcnt(2)
	v_add_f32_e32 v5, v5, v7
	s_waitcnt lgkmcnt(1)
	v_add_f32_e32 v3, v6, v3
	v_cndmask_b32_e64 v2, v2, v10, s[4:5]
	v_cndmask_b32_e32 v6, v5, v4, vcc
	v_cndmask_b32_e32 v4, v4, v5, vcc
	v_mov_b32_e32 v5, v155
	s_waitcnt lgkmcnt(0)
	v_add_f32_e32 v2, v2, v8
	v_mov_b32_dpp v5, v4 row_mirror row_mask:0xf bank_mask:0xf
	s_nop 1
	v_add_f32_dpp v4, v5, v6 row_half_mirror row_mask:0xf bank_mask:0xf bound_ctrl:1
	v_cndmask_b32_e32 v5, v2, v3, vcc
	v_cndmask_b32_e32 v2, v3, v2, vcc
	v_mov_b32_e32 v3, v155
	s_nop 1
	v_mov_b32_dpp v3, v2 row_mirror row_mask:0xf bank_mask:0xf
	s_nop 1
	v_add_f32_dpp v2, v3, v5 row_half_mirror row_mask:0xf bank_mask:0xf bound_ctrl:1
	v_cndmask_b32_e64 v3, v2, v4, s[0:1]
	v_cndmask_b32_e64 v2, v4, v2, s[0:1]
	v_mov_b32_e32 v4, v155
	s_nop 1
	v_mov_b32_dpp v4, v2 row_half_mirror row_mask:0xf bank_mask:0xf
	s_nop 1
	v_add_f32_dpp v2, v4, v3 quad_perm:[3,2,1,0] row_mask:0xf bank_mask:0xf bound_ctrl:1
	v_and_b32_e32 v4, 3, v156
	v_cmp_eq_u32_e32 vcc, 0, v4
	v_and_b32_e32 v4, 56, v156
	v_add_f32_dpp v2, v2, v2 quad_perm:[2,3,0,1] row_mask:0xf bank_mask:0xf bound_ctrl:1
	v_mov_b32_e32 v3, 0
	v_cmp_ne_u32_e64 s[0:1], 56, v4
	s_and_b64 s[2:3], vcc, s[0:1]
	v_mov_b32_dpp v3, v2 quad_perm:[1,0,3,2] row_mask:0xf bank_mask:0xf
	s_and_saveexec_b64 s[0:1], s[2:3]
	v_and_or_b32 v4, v156, 60, v165
	v_add_f32_e32 v2, v2, v3
	ds_add_f32 v4, v2
	s_or_b64 exec, exec, s[0:1]
	v_cmp_gt_i32_e32 vcc, 14, v156
	s_cmp_lt_i32 s22, 0
	s_cbranch_scc0 .Lno_stage
	s_waitcnt vmcnt(0)
	ds_write_b64 v194, v[190:191]
	s_cmp_lg_u32 s35, 0
	s_cbranch_scc1 .Lno_stage
	ds_write_b64 v194, v[192:193] offset:2048
.Lno_stage:
	s_waitcnt lgkmcnt(0)
	s_barrier
	s_and_saveexec_b64 s[0:1], vcc
	s_cbranch_execz .LBB1_2
	ds_read_b32 v2, v166
	s_waitcnt lgkmcnt(0)
	v_mul_f32_e32 v4, 0x39800000, v2
	v_lshl_add_u64 v[2:3], v[156:157], 2, s[14:15]
	global_store_dword v[2:3], v4, off
	s_branch .LBB1_2

	.amdhsa_kernel _Z9qsim_mainPKDF16_PK15HIP_vector_typeIfLj2EEPf
		.amdhsa_group_segment_fixed_size 68160
		.amdhsa_private_segment_fixed_size 0
		.amdhsa_kernarg_size 24
		.amdhsa_user_sgpr_count 2
		.amdhsa_user_sgpr_dispatch_ptr 0
		.amdhsa_user_sgpr_queue_ptr 0
		.amdhsa_user_sgpr_kernarg_segment_ptr 1
		.amdhsa_user_sgpr_dispatch_id 0
		.amdhsa_user_sgpr_kernarg_preload_length 0
		.amdhsa_user_sgpr_kernarg_preload_offset 0
		.amdhsa_user_sgpr_private_segment_size 0
		.amdhsa_uses_dynamic_stack 0
		.amdhsa_enable_private_segment 0
		.amdhsa_system_sgpr_workgroup_id_x 1
		.amdhsa_system_sgpr_workgroup_id_y 0
		.amdhsa_system_sgpr_workgroup_id_z 0
		.amdhsa_system_sgpr_workgroup_info 0
		.amdhsa_system_vgpr_workitem_id 0
		.amdhsa_next_free_vgpr 197
		.amdhsa_next_free_sgpr 96
		.amdhsa_accum_offset 200
		.amdhsa_reserve_vcc 1
		.amdhsa_float_round_mode_32 0
		.amdhsa_float_round_mode_16_64 0
		.amdhsa_float_denorm_mode_32 3
		.amdhsa_float_denorm_mode_16_64 3
		.amdhsa_dx10_clamp 1
		.amdhsa_ieee_mode 1
		.amdhsa_fp16_overflow 0
		.amdhsa_tg_split 0
		.amdhsa_exception_fp_ieee_invalid_op 0
		.amdhsa_exception_fp_denorm_src 0
		.amdhsa_exception_fp_ieee_div_zero 0
		.amdhsa_exception_fp_ieee_overflow 0
		.amdhsa_exception_fp_ieee_underflow 0
		.amdhsa_exception_fp_ieee_inexact 0
		.amdhsa_exception_int_div_zero 0
	.end_amdhsa_kernel

amdhsa.kernels:
  - .agpr_count:     0
    .args:
      - .actual_access:  read_only
        .address_space:  global
        .offset:         0
        .size:           8
        .value_kind:     global_buffer
      - .actual_access:  read_only
        .address_space:  global
        .offset:         8
        .size:           8
        .value_kind:     global_buffer
      - .actual_access:  read_only
        .address_space:  global
        .offset:         16
        .size:           8
        .value_kind:     global_buffer
      - .actual_access:  read_only
        .address_space:  global
        .offset:         24
        .size:           8
        .value_kind:     global_buffer
      - .actual_access:  write_only
        .address_space:  global
        .offset:         32
        .size:           8
        .value_kind:     global_buffer
      - .actual_access:  write_only
        .address_space:  global
        .offset:         40
        .size:           8
        .value_kind:     global_buffer
    .group_segment_fixed_size: 1920
    .kernarg_segment_align: 8
    .kernarg_segment_size: 48
    .language:       OpenCL C
    .language_version:
      - 2
      - 0
    .max_flat_workgroup_size: 256
    .name:           _Z11prep_kernelPKfS0_S0_S0_PDF16_P15HIP_vector_typeIfLj2EE
    .private_segment_fixed_size: 0
    .sgpr_count:     22
    .sgpr_spill_count: 0
    .symbol:         _Z11prep_kernelPKfS0_S0_S0_PDF16_P15HIP_vector_typeIfLj2EE.kd
    .uniform_work_group_size: 1
    .uses_dynamic_stack: false
    .vgpr_count:     59
    .vgpr_spill_count: 0
    .wavefront_size: 64
  - .agpr_count:     0
    .args:
      - .actual_access:  read_only
        .address_space:  global
        .offset:         0
        .size:           8
        .value_kind:     global_buffer
      - .actual_access:  read_only
        .address_space:  global
        .offset:         8
        .size:           8
        .value_kind:     global_buffer
      - .actual_access:  write_only
        .address_space:  global
        .offset:         16
        .size:           8
        .value_kind:     global_buffer
    .group_segment_fixed_size: 68160
    .kernarg_segment_align: 8
    .kernarg_segment_size: 24
    .language:       OpenCL C
    .language_version:
      - 2
      - 0
    .max_flat_workgroup_size: 256
    .name:           _Z9qsim_mainPKDF16_PK15HIP_vector_typeIfLj2EEPf
    .private_segment_fixed_size: 0
    .sgpr_count:     41
    .sgpr_spill_count: 0
    .symbol:         _Z9qsim_mainPKDF16_PK15HIP_vector_typeIfLj2EEPf.kd
    .uniform_work_group_size: 1
    .uses_dynamic_stack: false
    .vgpr_count:     197
    .vgpr_spill_count: 0
    .wavefront_size: 64
